# LN1 / LN2 / x-quantisation wave reductions: serial ds_bpermute butterflies replaced by DPP moves + permlane16/32_swap (P6, P10, P0a), on top of v70
# speedup vs baseline: 1.0148x; 1.0025x over previous
.LBB0_8:
	v_ashrrev_i32_e32 v35, 31, v34
	v_lshlrev_b64 v[2:3], 13, v[34:35]
	v_lshl_add_u64 v[2:3], v[36:37], 0, v[2:3]
	global_load_dwordx4 v[26:29], v[2:3], off offset:16 nt
	global_load_dwordx4 v[30:33], v[2:3], off nt
	global_load_dwordx4 v[18:21], v[2:3], off offset:2064 nt
	global_load_dwordx4 v[22:25], v[2:3], off offset:2048 nt
	v_add_co_u32_e32 v48, vcc, s1, v2
	v_lshl_add_u64 v[4:5], v[2:3], 0, s[26:27]
	s_nop 0
	v_addc_co_u32_e32 v49, vcc, 0, v3, vcc
	global_load_dwordx4 v[14:17], v[48:49], off nt
	global_load_dwordx4 v[10:13], v[4:5], off offset:16 nt
	v_lshl_add_u64 v[50:51], v[2:3], 0, s[28:29]
	global_load_dwordx4 v[6:9], v[48:49], off offset:2048 nt
	global_load_dwordx4 v[2:5], v[50:51], off offset:16 nt
	s_waitcnt vmcnt(7)
	v_max_f32_e64 v48, |v26|, |v26|
	s_waitcnt vmcnt(6)
	v_max_f32_e64 v49, |v30|, |v30|
	v_max_f32_e64 v50, |v27|, |v27|
	v_max_f32_e64 v51, |v31|, |v31|
	v_max_f32_e64 v52, |v28|, |v28|
	v_max_f32_e64 v53, |v32|, |v32|
	v_max_f32_e64 v54, |v29|, |v29|
	v_max_f32_e64 v55, |v33|, |v33|
	v_max_f32_e32 v48, v49, v48
	v_max_f32_e32 v49, v51, v50
	s_waitcnt vmcnt(5)
	v_max_f32_e64 v56, |v18|, |v18|
	s_waitcnt vmcnt(4)
	v_max_f32_e64 v57, |v22|, |v22|
	v_max_f32_e64 v58, |v19|, |v19|
	v_max_f32_e64 v59, |v23|, |v23|
	v_max_f32_e32 v50, v53, v52
	v_max_f32_e32 v51, v55, v54
	v_max3_f32 v48, v48, 0, v49
	v_max_f32_e64 v60, |v20|, |v20|
	v_max_f32_e64 v61, |v24|, |v24|
	v_max_f32_e64 v62, |v21|, |v21|
	v_max_f32_e64 v63, |v25|, |v25|
	v_max_f32_e32 v52, v57, v56
	v_max_f32_e32 v53, v59, v58
	v_max3_f32 v48, v48, v50, v51
	v_max_f32_e32 v54, v61, v60
	v_max_f32_e32 v55, v63, v62
	s_waitcnt vmcnt(3)
	v_max_f32_e64 v56, |v14|, |v14|
	s_waitcnt vmcnt(2)
	v_max_f32_e64 v57, |v10|, |v10|
	v_max_f32_e64 v58, |v15|, |v15|
	v_max_f32_e64 v59, |v11|, |v11|
	v_max3_f32 v48, v48, v52, v53
	v_max_f32_e64 v60, |v16|, |v16|
	v_max_f32_e64 v61, |v12|, |v12|
	v_max_f32_e64 v62, |v17|, |v17|
	v_max_f32_e64 v63, |v13|, |v13|
	v_max_f32_e32 v49, v56, v57
	v_max_f32_e32 v56, v58, v59
	v_max3_f32 v48, v48, v54, v55
	s_waitcnt vmcnt(1)
	v_max_f32_e64 v64, |v6|, |v6|
	s_waitcnt vmcnt(0)
	v_max_f32_e64 v65, |v2|, |v2|
	v_max_f32_e64 v66, |v7|, |v7|
	v_max_f32_e64 v67, |v3|, |v3|
	v_max_f32_e32 v57, v60, v61
	v_max_f32_e32 v58, v62, v63
	v_max3_f32 v48, v48, v49, v56
	v_max_f32_e64 v68, |v8|, |v8|
	v_max_f32_e64 v69, |v4|, |v4|
	v_max_f32_e64 v70, |v9|, |v9|
	v_max_f32_e64 v71, |v5|, |v5|
	v_max_f32_e32 v59, v64, v65
	v_max_f32_e32 v60, v66, v67
	v_max3_f32 v48, v48, v57, v58
	v_max_f32_e32 v61, v68, v69
	v_max3_f32 v48, v48, v59, v60
	v_max_f32_e32 v49, v70, v71
	v_max3_f32 v48, v48, v61, v49
	v_mov_b32_e32 v49, v48
	s_nop 1
	v_permlane32_swap_b32_e32 v49, v48
	s_waitcnt lgkmcnt(0)
	v_max_f32_e32 v49, v49, v49
	v_max_f32_e32 v48, v48, v49
	v_mov_b32_e32 v49, v48
	s_nop 1
	v_permlane16_swap_b32_e32 v49, v48
	s_waitcnt lgkmcnt(0)
	v_max_f32_e32 v49, v49, v49
	v_max_f32_e32 v48, v48, v49
	s_nop 1
	v_mov_b32_dpp v49, v48 row_ror:8 row_mask:0xf bank_mask:0xf
	s_waitcnt lgkmcnt(0)
	v_max_f32_e32 v49, v49, v49
	v_max_f32_e32 v48, v48, v49
	s_nop 1
	v_mov_b32_dpp v49, v48 row_shr:4 row_mask:0xf bank_mask:0xa
	v_mov_b32_dpp v49, v48 row_shl:4 row_mask:0xf bank_mask:0x5
	s_waitcnt lgkmcnt(0)
	v_max_f32_e32 v49, v49, v49
	v_max_f32_e32 v48, v48, v49
	s_nop 1
	v_mov_b32_dpp v49, v48 quad_perm:[2,3,0,1] row_mask:0xf bank_mask:0xf
	s_waitcnt lgkmcnt(0)
	v_max_f32_e32 v49, v49, v49
	v_max_f32_e32 v48, v48, v49
	s_nop 1
	v_mov_b32_dpp v49, v48 quad_perm:[1,0,3,2] row_mask:0xf bank_mask:0xf
	s_waitcnt lgkmcnt(0)
	v_max_f32_e32 v49, v49, v49
	v_max_f32_e32 v48, v48, v49
	s_and_saveexec_b64 s[30:31], s[6:7]
	s_cbranch_execz .LBB0_7
	v_lshl_add_u64 v[50:51], v[34:35], 2, s[24:25]
	v_mul_f32_e32 v49, 0x3c010204, v48
	global_store_dword v[50:51], v49, off
	s_branch .LBB0_7

.LBB0_1026:
	v_or_b32_e32 v52, s0, v83
	v_ashrrev_i32_e32 v53, 31, v52
	v_lshlrev_b64 v[50:51], 12, v[52:53]
	v_lshl_add_u64 v[2:3], v[72:73], 0, v[50:51]
	global_load_dwordx4 v[88:91], v[2:3], off
	global_load_dwordx4 v[96:99], v[2:3], off offset:1024
	global_load_dwordx4 v[236:239], v[2:3], off offset:2048
	global_load_dwordx4 v[240:243], v[2:3], off offset:3072
	v_or_b32_e32 v86, 1, v52
	v_ashrrev_i32_e32 v87, 31, v86
	v_or_b32_e32 v64, 2, v52
	v_lshlrev_b64 v[84:85], 12, v[86:87]
	v_ashrrev_i32_e32 v65, 31, v64
	v_or_b32_e32 v60, 3, v52
	v_lshl_add_u64 v[2:3], v[72:73], 0, v[84:85]
	v_lshlrev_b64 v[62:63], 12, v[64:65]
	v_ashrrev_i32_e32 v61, 31, v60
	global_load_dwordx4 v[46:49], v[2:3], off
	global_load_dwordx4 v[42:45], v[2:3], off offset:1024
	global_load_dwordx4 v[38:41], v[2:3], off offset:2048
	global_load_dwordx4 v[34:37], v[2:3], off offset:3072
	v_lshl_add_u64 v[2:3], v[72:73], 0, v[62:63]
	v_lshlrev_b64 v[58:59], 12, v[60:61]
	global_load_dwordx4 v[30:33], v[2:3], off
	global_load_dwordx4 v[26:29], v[2:3], off offset:1024
	global_load_dwordx4 v[22:25], v[2:3], off offset:2048
	global_load_dwordx4 v[18:21], v[2:3], off offset:3072
	v_lshl_add_u64 v[2:3], v[72:73], 0, v[58:59]
	global_load_dwordx4 v[14:17], v[2:3], off
	global_load_dwordx4 v[10:13], v[2:3], off offset:1024
	global_load_dwordx4 v[6:9], v[2:3], off offset:2048
	s_nop 0
	global_load_dwordx4 v[2:5], v[2:3], off offset:3072
	v_lshlrev_b64 v[52:53], 11, v[52:53]
	s_waitcnt vmcnt(15)
	v_lshlrev_b32_e32 v94, 16, v88
	v_and_b32_e32 v92, 0xffff0000, v88
	v_add_f32_e32 v88, 0, v94
	v_lshlrev_b32_e32 v56, 16, v89
	v_add_f32_e32 v88, v88, v92
	v_and_b32_e32 v54, 0xffff0000, v89
	v_add_f32_e32 v88, v88, v56
	v_lshlrev_b32_e32 v95, 16, v90
	v_add_f32_e32 v88, v88, v54
	v_and_b32_e32 v93, 0xffff0000, v90
	v_add_f32_e32 v88, v88, v95
	v_lshlrev_b32_e32 v57, 16, v91
	v_add_f32_e32 v88, v88, v93
	v_and_b32_e32 v55, 0xffff0000, v91
	v_add_f32_e32 v88, v88, v57
	s_waitcnt vmcnt(14)
	v_lshlrev_b32_e32 v235, 16, v96
	v_add_f32_e32 v88, v88, v55
	v_and_b32_e32 v233, 0xffff0000, v96
	v_add_f32_e32 v88, v88, v235
	v_lshlrev_b32_e32 v231, 16, v97
	v_add_f32_e32 v88, v88, v233
	v_and_b32_e32 v228, 0xffff0000, v97
	v_add_f32_e32 v88, v88, v231
	v_lshlrev_b32_e32 v234, 16, v98
	v_add_f32_e32 v88, v88, v228
	v_and_b32_e32 v232, 0xffff0000, v98
	v_add_f32_e32 v88, v88, v234
	v_lshlrev_b32_e32 v230, 16, v99
	v_add_f32_e32 v88, v88, v232
	v_and_b32_e32 v229, 0xffff0000, v99
	v_add_f32_e32 v88, v88, v230
	s_waitcnt vmcnt(13)
	v_lshlrev_b32_e32 v226, 16, v236
	v_add_f32_e32 v88, v88, v229
	v_and_b32_e32 v224, 0xffff0000, v236
	v_add_f32_e32 v88, v88, v226
	v_lshlrev_b32_e32 v222, 16, v237
	v_add_f32_e32 v88, v88, v224
	v_and_b32_e32 v100, 0xffff0000, v237
	v_add_f32_e32 v88, v88, v222
	v_lshlrev_b32_e32 v227, 16, v238
	v_add_f32_e32 v88, v88, v100
	v_and_b32_e32 v225, 0xffff0000, v238
	v_add_f32_e32 v88, v88, v227
	v_lshlrev_b32_e32 v223, 16, v239
	v_add_f32_e32 v88, v88, v225
	v_and_b32_e32 v101, 0xffff0000, v239
	v_add_f32_e32 v88, v88, v223
	s_waitcnt vmcnt(12)
	v_lshlrev_b32_e32 v99, 16, v240
	v_add_f32_e32 v88, v88, v101
	v_and_b32_e32 v98, 0xffff0000, v240
	v_add_f32_e32 v88, v88, v99
	v_lshlrev_b32_e32 v97, 16, v241
	v_add_f32_e32 v88, v88, v98
	v_and_b32_e32 v96, 0xffff0000, v241
	v_add_f32_e32 v88, v88, v97
	v_add_f32_e32 v122, v88, v96
	v_lshlrev_b32_e32 v91, 16, v242
	v_and_b32_e32 v90, 0xffff0000, v242
	v_add_f32_e32 v122, v122, v91
	v_lshlrev_b32_e32 v89, 16, v243
	v_add_f32_e32 v122, v122, v90
	v_and_b32_e32 v88, 0xffff0000, v243
	v_add_f32_e32 v122, v122, v89
	v_add_f32_e32 v122, v122, v88
	v_mov_b32_e32 v123, v122
	s_nop 1
	v_permlane32_swap_b32_e32 v123, v122
	s_waitcnt lgkmcnt(0)
	v_add_f32_e32 v122, v122, v123
	v_mov_b32_e32 v123, v122
	s_nop 1
	v_permlane16_swap_b32_e32 v123, v122
	s_waitcnt lgkmcnt(0)
	v_add_f32_e32 v122, v122, v123
	s_nop 1
	v_mov_b32_dpp v123, v122 row_ror:8 row_mask:0xf bank_mask:0xf
	s_waitcnt lgkmcnt(0)
	v_add_f32_e32 v122, v122, v123
	s_nop 1
	v_mov_b32_dpp v123, v122 row_shr:4 row_mask:0xf bank_mask:0xa
	v_mov_b32_dpp v123, v122 row_shl:4 row_mask:0xf bank_mask:0x5
	s_waitcnt lgkmcnt(0)
	v_add_f32_e32 v122, v122, v123
	s_nop 1
	v_mov_b32_dpp v123, v122 quad_perm:[2,3,0,1] row_mask:0xf bank_mask:0xf
	s_waitcnt lgkmcnt(0)
	v_add_f32_e32 v122, v122, v123
	s_nop 1
	v_mov_b32_dpp v123, v122 quad_perm:[1,0,3,2] row_mask:0xf bank_mask:0xf
	s_waitcnt lgkmcnt(0)
	v_add_f32_e32 v122, v122, v123
	v_fmamk_f32 v236, v122, 0xba000000, v92
	v_fmamk_f32 v123, v122, 0xba000000, v94
	v_mul_f32_e32 v239, v236, v236
	v_fmac_f32_e32 v239, v123, v123
	v_fmamk_f32 v123, v122, 0xba000000, v56
	v_fmac_f32_e32 v239, v123, v123
	v_fmamk_f32 v123, v122, 0xba000000, v54
	v_fmac_f32_e32 v239, v123, v123
	v_fmamk_f32 v123, v122, 0xba000000, v95
	v_fmac_f32_e32 v239, v123, v123
	v_fmamk_f32 v123, v122, 0xba000000, v93
	v_fmac_f32_e32 v239, v123, v123
	v_fmamk_f32 v123, v122, 0xba000000, v57
	v_fmac_f32_e32 v239, v123, v123
	v_fmamk_f32 v123, v122, 0xba000000, v55
	v_fmac_f32_e32 v239, v123, v123
	v_fmamk_f32 v123, v122, 0xba000000, v235
	v_fmac_f32_e32 v239, v123, v123
	v_fmamk_f32 v123, v122, 0xba000000, v233
	v_fmac_f32_e32 v239, v123, v123
	v_fmamk_f32 v123, v122, 0xba000000, v231
	v_fmac_f32_e32 v239, v123, v123
	v_fmamk_f32 v123, v122, 0xba000000, v228
	v_fmac_f32_e32 v239, v123, v123
	v_fmamk_f32 v123, v122, 0xba000000, v234
	v_fmac_f32_e32 v239, v123, v123
	v_fmamk_f32 v123, v122, 0xba000000, v232
	v_fmac_f32_e32 v239, v123, v123
	v_fmamk_f32 v123, v122, 0xba000000, v230
	v_fmac_f32_e32 v239, v123, v123
	v_fmamk_f32 v123, v122, 0xba000000, v229
	v_fmac_f32_e32 v239, v123, v123
	v_fmamk_f32 v123, v122, 0xba000000, v226
	v_fmac_f32_e32 v239, v123, v123
	v_fmamk_f32 v123, v122, 0xba000000, v224
	v_fmac_f32_e32 v239, v123, v123
	v_fmamk_f32 v123, v122, 0xba000000, v222
	v_fmac_f32_e32 v239, v123, v123
	v_fmamk_f32 v123, v122, 0xba000000, v100
	v_fmac_f32_e32 v239, v123, v123
	v_fmamk_f32 v123, v122, 0xba000000, v227
	v_fmac_f32_e32 v239, v123, v123
	v_fmamk_f32 v123, v122, 0xba000000, v225
	v_fmac_f32_e32 v239, v123, v123
	v_fmamk_f32 v123, v122, 0xba000000, v223
	v_fmac_f32_e32 v239, v123, v123
	v_fmamk_f32 v123, v122, 0xba000000, v101
	v_fmac_f32_e32 v239, v123, v123
	v_fmamk_f32 v123, v122, 0xba000000, v99
	v_fmac_f32_e32 v239, v123, v123
	v_fmamk_f32 v123, v122, 0xba000000, v98
	v_fmac_f32_e32 v239, v123, v123
	v_fmamk_f32 v123, v122, 0xba000000, v97
	v_mul_f32_e32 v238, 0x3a000000, v122
	v_fmac_f32_e32 v239, v123, v123
	v_fmamk_f32 v122, v122, 0xba000000, v96
	v_fmac_f32_e32 v239, v122, v122
	v_pk_add_f32 v[236:237], v[90:91], v[238:239] op_sel_hi:[1,0] neg_lo:[0,1] neg_hi:[0,1]
	s_nop 0
	v_pk_mul_f32 v[236:237], v[236:237], v[236:237]
	s_nop 0
	v_add_f32_e32 v122, v237, v239
	v_add_f32_e32 v122, v236, v122
	v_pk_add_f32 v[236:237], v[88:89], v[238:239] op_sel_hi:[1,0] neg_lo:[0,1] neg_hi:[0,1]
	s_nop 0
	v_pk_mul_f32 v[236:237], v[236:237], v[236:237]
	s_nop 0
	v_add_f32_e32 v122, v237, v122
	v_add_f32_e32 v122, v236, v122
	v_mov_b32_e32 v123, v122
	s_nop 1
	v_permlane32_swap_b32_e32 v123, v122
	s_waitcnt lgkmcnt(0)
	v_add_f32_e32 v122, v122, v123
	v_mov_b32_e32 v123, v122
	s_nop 1
	v_permlane16_swap_b32_e32 v123, v122
	s_waitcnt lgkmcnt(0)
	v_add_f32_e32 v122, v122, v123
	s_nop 1
	v_mov_b32_dpp v123, v122 row_ror:8 row_mask:0xf bank_mask:0xf
	s_waitcnt lgkmcnt(0)
	v_add_f32_e32 v122, v122, v123
	s_nop 1
	v_mov_b32_dpp v123, v122 row_shr:4 row_mask:0xf bank_mask:0xa
	v_mov_b32_dpp v123, v122 row_shl:4 row_mask:0xf bank_mask:0x5
	s_waitcnt lgkmcnt(0)
	v_add_f32_e32 v122, v122, v123
	s_nop 1
	v_mov_b32_dpp v123, v122 quad_perm:[2,3,0,1] row_mask:0xf bank_mask:0xf
	s_waitcnt lgkmcnt(0)
	v_add_f32_e32 v122, v122, v123
	s_nop 1
	v_mov_b32_dpp v123, v122 quad_perm:[1,0,3,2] row_mask:0xf bank_mask:0xf
	s_waitcnt lgkmcnt(0)
	v_add_f32_e32 v122, v122, v123
	v_fmamk_f32 v122, v122, 0x3a000000, v219
	v_cmp_gt_f32_e32 vcc, s33, v122
	v_mul_f32_e32 v123, 0x4b800000, v122
	s_nop 0
	v_cndmask_b32_e32 v122, v122, v123, vcc
	v_rsq_f32_e32 v122, v122
	s_nop 0
	v_mul_f32_e32 v123, 0x45800000, v122
	v_cndmask_b32_e32 v236, v122, v123, vcc
	v_mul_f32_e64 v237, v236, -v238
	ds_read_b128 v[238:241], v112 offset:4096
	ds_read_b128 v[242:245], v112 offset:4112
	ds_read_b128 v[246:249], v112 offset:12288
	ds_read_b128 v[250:253], v112 offset:12304
	v_fma_f32 v94, v94, v236, v237
	v_fma_f32 v92, v92, v236, v237
	v_fma_f32 v93, v93, v236, v237
	s_waitcnt lgkmcnt(1)
	v_fma_f32 v122, v94, v238, v246
	v_fma_f32 v94, v95, v236, v237
	v_fma_f32 v56, v56, v236, v237
	v_fma_f32 v54, v54, v236, v237
	s_waitcnt lgkmcnt(0)
	v_fma_f32 v123, v94, v242, v250
	v_fma_f32 v92, v92, v239, v247
	v_fma_f32 v93, v93, v243, v251
	v_fma_f32 v238, v56, v240, v248
	v_fma_f32 v56, v57, v236, v237
	v_fmac_f32_e32 v249, v54, v241
	v_fma_f32 v54, v55, v236, v237
	v_fma_f32 v239, v56, v244, v252
	v_fmac_f32_e32 v253, v54, v245
	v_cvt_pk_bf16_f32 v54, v122, v92
	v_cvt_pk_bf16_f32 v55, v238, v249
	v_cvt_pk_bf16_f32 v56, v123, v93
	v_cvt_pk_fp8_f32 v122, v122, v92
	v_cvt_pk_fp8_f32 v123, v123, v93
	v_lshl_add_u64 v[94:95], v[76:77], 0, v[50:51]
	v_lshl_add_u64 v[92:93], v[78:79], 0, v[52:53]
	v_cvt_pk_fp8_f32 v122, v238, v249 op_sel:[0,0,1]
	v_cvt_pk_fp8_f32 v123, v239, v253 op_sel:[0,0,1]
	v_cvt_pk_bf16_f32 v57, v239, v253
	global_store_dwordx4 v[94:95], v[54:57], off
	v_fma_f32 v99, v99, v236, v237
	global_store_dwordx2 v[92:93], v[122:123], off
	ds_read_b128 v[238:241], v112 offset:6144
	ds_read_b128 v[242:245], v112 offset:6160
	ds_read_b128 v[54:57], v112 offset:14336
	ds_read_b128 v[50:53], v112 offset:14352
	v_fma_f32 v122, v235, v236, v237
	s_waitcnt lgkmcnt(1)
	v_fma_f32 v122, v122, v238, v54
	v_fma_f32 v54, v234, v236, v237
	s_waitcnt lgkmcnt(0)
	v_fma_f32 v123, v54, v242, v50
	v_fma_f32 v50, v233, v236, v237
	v_fma_f32 v50, v50, v239, v55
	v_fma_f32 v54, v232, v236, v237
	v_fma_f32 v55, v230, v236, v237
	v_fma_f32 v51, v54, v243, v51
	v_fma_f32 v54, v231, v236, v237
	v_fma_f32 v52, v55, v244, v52
	v_fma_f32 v55, v228, v236, v237
	v_fma_f32 v54, v54, v240, v56
	v_fmac_f32_e32 v57, v55, v241
	v_fma_f32 v55, v229, v236, v237
	v_cvt_pk_bf16_f32 v228, v122, v50
	v_cvt_pk_bf16_f32 v229, v54, v57
	v_cvt_pk_bf16_f32 v230, v123, v51
	v_cvt_pk_fp8_f32 v122, v122, v50
	v_cvt_pk_fp8_f32 v123, v123, v51
	v_fmac_f32_e32 v53, v55, v245
	v_cvt_pk_bf16_f32 v231, v52, v53
	v_cvt_pk_fp8_f32 v122, v54, v57 op_sel:[0,0,1]
	v_cvt_pk_fp8_f32 v123, v52, v53 op_sel:[0,0,1]
	global_store_dwordx4 v[94:95], v[228:231], off offset:1024
	global_store_dwordx2 v[92:93], v[122:123], off offset:512
	ds_read_b128 v[50:53], v112 offset:8192
	ds_read_b128 v[54:57], v112 offset:8208
	ds_read_b128 v[228:231], v112 offset:16384
	ds_read_b128 v[232:235], v112 offset:16400
	v_fma_f32 v122, v226, v236, v237
	s_waitcnt lgkmcnt(1)
	v_fma_f32 v122, v122, v50, v228
	v_fma_f32 v50, v227, v236, v237
	s_waitcnt lgkmcnt(0)
	v_fma_f32 v123, v50, v54, v232
	v_fma_f32 v50, v224, v236, v237
	v_fma_f32 v54, v50, v51, v229
	v_fma_f32 v50, v225, v236, v237
	v_fma_f32 v55, v50, v55, v233
	v_fma_f32 v50, v222, v236, v237
	v_fma_f32 v222, v50, v52, v230
	v_fma_f32 v50, v223, v236, v237
	v_fma_f32 v56, v50, v56, v234
	v_fma_f32 v50, v100, v236, v237
	v_fmac_f32_e32 v231, v50, v53
	v_fma_f32 v50, v101, v236, v237
	v_fmac_f32_e32 v235, v50, v57
	v_cvt_pk_bf16_f32 v50, v122, v54
	v_cvt_pk_bf16_f32 v51, v222, v231
	v_cvt_pk_bf16_f32 v52, v123, v55
	v_cvt_pk_fp8_f32 v122, v122, v54
	v_cvt_pk_fp8_f32 v123, v123, v55
	v_cvt_pk_bf16_f32 v53, v56, v235
	global_store_dwordx4 v[94:95], v[50:53], off offset:2048
	v_cvt_pk_fp8_f32 v122, v222, v231 op_sel:[0,0,1]
	v_cvt_pk_fp8_f32 v123, v56, v235 op_sel:[0,0,1]
	global_store_dwordx2 v[92:93], v[122:123], off offset:1024
	ds_read_b128 v[50:53], v112 offset:10240
	ds_read_b128 v[54:57], v112 offset:10256
	ds_read_b128 v[222:225], v112 offset:18432
	ds_read_b128 v[226:229], v112 offset:18448
	s_waitcnt lgkmcnt(1)
	v_fma_f32 v100, v99, v50, v222
	v_fma_f32 v50, v91, v236, v237
	s_waitcnt lgkmcnt(0)
	v_fma_f32 v101, v50, v54, v226
	v_fma_f32 v50, v98, v236, v237
	v_fma_f32 v54, v50, v51, v223
	v_fma_f32 v50, v90, v236, v237
	v_fma_f32 v55, v50, v55, v227
	v_fma_f32 v50, v97, v236, v237
	v_fma_f32 v90, v50, v52, v224
	v_fma_f32 v50, v89, v236, v237
	v_fma_f32 v56, v50, v56, v228
	v_fma_f32 v50, v96, v236, v237
	v_fmac_f32_e32 v225, v50, v53
	v_cvt_pk_bf16_f32 v50, v100, v54
	v_cvt_pk_bf16_f32 v51, v90, v225
	v_cvt_pk_bf16_f32 v52, v101, v55
	v_cvt_pk_fp8_f32 v100, v100, v54
	v_cvt_pk_fp8_f32 v101, v101, v55
	v_fmac_f32_e32 v237, v88, v236
	v_fmac_f32_e32 v229, v237, v57
	v_cvt_pk_fp8_f32 v100, v90, v225 op_sel:[0,0,1]
	v_cvt_pk_fp8_f32 v101, v56, v229 op_sel:[0,0,1]
	v_cvt_pk_bf16_f32 v53, v56, v229
	global_store_dwordx4 v[94:95], v[50:53], off offset:3072
	global_store_dwordx2 v[92:93], v[100:101], off offset:1536
	s_waitcnt vmcnt(19)
	v_lshlrev_b32_e32 v56, 16, v46
	v_and_b32_e32 v88, 0xffff0000, v46
	s_waitcnt vmcnt(16)
	v_lshlrev_b32_e32 v228, 16, v34
	v_and_b32_e32 v229, 0xffff0000, v34
	v_add_f32_e32 v34, 0, v56
	v_lshlrev_b32_e32 v89, 16, v47
	v_add_f32_e32 v34, v34, v88
	v_and_b32_e32 v90, 0xffff0000, v47
	v_add_f32_e32 v34, v34, v89
	v_lshlrev_b32_e32 v57, 16, v48
	v_add_f32_e32 v34, v34, v90
	v_and_b32_e32 v91, 0xffff0000, v48
	v_add_f32_e32 v34, v34, v57
	v_lshlrev_b32_e32 v92, 16, v49
	v_add_f32_e32 v34, v34, v91
	v_and_b32_e32 v93, 0xffff0000, v49
	v_add_f32_e32 v34, v34, v92
	v_lshlrev_b32_e32 v94, 16, v42
	v_add_f32_e32 v34, v34, v93
	v_and_b32_e32 v95, 0xffff0000, v42
	v_add_f32_e32 v34, v34, v94
	v_lshlrev_b32_e32 v96, 16, v43
	v_add_f32_e32 v34, v34, v95
	v_and_b32_e32 v97, 0xffff0000, v43
	v_add_f32_e32 v34, v34, v96
	v_lshlrev_b32_e32 v98, 16, v44
	v_add_f32_e32 v34, v34, v97
	v_and_b32_e32 v99, 0xffff0000, v44
	v_add_f32_e32 v34, v34, v98
	v_lshlrev_b32_e32 v100, 16, v45
	v_add_f32_e32 v34, v34, v99
	v_and_b32_e32 v101, 0xffff0000, v45
	v_add_f32_e32 v34, v34, v100
	v_lshlrev_b32_e32 v122, 16, v38
	v_add_f32_e32 v34, v34, v101
	v_and_b32_e32 v123, 0xffff0000, v38
	v_add_f32_e32 v34, v34, v122
	v_lshlrev_b32_e32 v222, 16, v39
	v_add_f32_e32 v34, v34, v123
	v_and_b32_e32 v223, 0xffff0000, v39
	v_add_f32_e32 v34, v34, v222
	v_lshlrev_b32_e32 v224, 16, v40
	v_add_f32_e32 v34, v34, v223
	v_and_b32_e32 v225, 0xffff0000, v40
	v_add_f32_e32 v34, v34, v224
	v_lshlrev_b32_e32 v226, 16, v41
	v_add_f32_e32 v34, v34, v225
	v_and_b32_e32 v227, 0xffff0000, v41
	v_add_f32_e32 v34, v34, v226
	v_add_f32_e32 v34, v34, v227
	v_add_f32_e32 v34, v34, v228
	v_lshlrev_b32_e32 v230, 16, v35
	v_add_f32_e32 v34, v34, v229
	v_and_b32_e32 v231, 0xffff0000, v35
	v_add_f32_e32 v34, v34, v230
	v_add_f32_e32 v40, v34, v231
	v_lshlrev_b32_e32 v39, 16, v36
	v_and_b32_e32 v38, 0xffff0000, v36
	v_add_f32_e32 v36, v40, v39
	v_lshlrev_b32_e32 v35, 16, v37
	v_add_f32_e32 v36, v36, v38
	v_and_b32_e32 v34, 0xffff0000, v37
	v_add_f32_e32 v36, v36, v35
	v_add_f32_e32 v36, v36, v34
	v_mov_b32_e32 v37, v36
	s_nop 1
	v_permlane32_swap_b32_e32 v37, v36
	v_lshl_add_u64 v[84:85], v[76:77], 0, v[84:85]
	s_waitcnt lgkmcnt(0)
	v_add_f32_e32 v36, v36, v37
	v_mov_b32_e32 v37, v36
	s_nop 1
	v_permlane16_swap_b32_e32 v37, v36
	s_waitcnt lgkmcnt(0)
	v_add_f32_e32 v36, v36, v37
	s_nop 1
	v_mov_b32_dpp v37, v36 row_ror:8 row_mask:0xf bank_mask:0xf
	s_waitcnt lgkmcnt(0)
	v_add_f32_e32 v36, v36, v37
	s_nop 1
	v_mov_b32_dpp v37, v36 row_shr:4 row_mask:0xf bank_mask:0xa
	v_mov_b32_dpp v37, v36 row_shl:4 row_mask:0xf bank_mask:0x5
	s_waitcnt lgkmcnt(0)
	v_add_f32_e32 v36, v36, v37
	s_nop 1
	v_mov_b32_dpp v37, v36 quad_perm:[2,3,0,1] row_mask:0xf bank_mask:0xf
	s_waitcnt lgkmcnt(0)
	v_add_f32_e32 v36, v36, v37
	s_nop 1
	v_mov_b32_dpp v37, v36 quad_perm:[1,0,3,2] row_mask:0xf bank_mask:0xf
	s_waitcnt lgkmcnt(0)
	v_add_f32_e32 v37, v36, v37
	v_fmamk_f32 v41, v37, 0xba000000, v88
	v_fmamk_f32 v40, v37, 0xba000000, v56
	v_mul_f32_e32 v42, v41, v41
	v_fmac_f32_e32 v42, v40, v40
	v_fmamk_f32 v40, v37, 0xba000000, v89
	v_fmac_f32_e32 v42, v40, v40
	v_fmamk_f32 v40, v37, 0xba000000, v90
	v_fmac_f32_e32 v42, v40, v40
	v_fmamk_f32 v40, v37, 0xba000000, v57
	v_fmac_f32_e32 v42, v40, v40
	v_fmamk_f32 v40, v37, 0xba000000, v91
	v_fmac_f32_e32 v42, v40, v40
	v_fmamk_f32 v40, v37, 0xba000000, v92
	v_fmac_f32_e32 v42, v40, v40
	v_fmamk_f32 v40, v37, 0xba000000, v93
	v_fmac_f32_e32 v42, v40, v40
	v_fmamk_f32 v40, v37, 0xba000000, v94
	v_fmac_f32_e32 v42, v40, v40
	v_fmamk_f32 v40, v37, 0xba000000, v95
	v_fmac_f32_e32 v42, v40, v40
	v_fmamk_f32 v40, v37, 0xba000000, v96
	v_fmac_f32_e32 v42, v40, v40
	v_fmamk_f32 v40, v37, 0xba000000, v97
	v_fmac_f32_e32 v42, v40, v40
	v_fmamk_f32 v40, v37, 0xba000000, v98
	v_fmac_f32_e32 v42, v40, v40
	v_fmamk_f32 v40, v37, 0xba000000, v99
	v_fmac_f32_e32 v42, v40, v40
	v_fmamk_f32 v40, v37, 0xba000000, v100
	v_fmac_f32_e32 v42, v40, v40
	v_fmamk_f32 v40, v37, 0xba000000, v101
	v_fmac_f32_e32 v42, v40, v40
	v_fmamk_f32 v40, v37, 0xba000000, v122
	v_fmac_f32_e32 v42, v40, v40
	v_fmamk_f32 v40, v37, 0xba000000, v123
	v_fmac_f32_e32 v42, v40, v40
	v_fmamk_f32 v40, v37, 0xba000000, v222
	v_fmac_f32_e32 v42, v40, v40
	v_fmamk_f32 v40, v37, 0xba000000, v223
	v_fmac_f32_e32 v42, v40, v40
	v_fmamk_f32 v40, v37, 0xba000000, v224
	v_fmac_f32_e32 v42, v40, v40
	v_fmamk_f32 v40, v37, 0xba000000, v225
	v_fmac_f32_e32 v42, v40, v40
	v_fmamk_f32 v40, v37, 0xba000000, v226
	v_fmac_f32_e32 v42, v40, v40
	v_fmamk_f32 v40, v37, 0xba000000, v227
	v_fmac_f32_e32 v42, v40, v40
	v_fmamk_f32 v40, v37, 0xba000000, v228
	v_fmac_f32_e32 v42, v40, v40
	v_fmamk_f32 v40, v37, 0xba000000, v229
	v_mul_f32_e32 v36, 0x3a000000, v37
	v_fmac_f32_e32 v42, v40, v40
	v_fmamk_f32 v40, v37, 0xba000000, v230
	v_fmamk_f32 v37, v37, 0xba000000, v231
	v_fmac_f32_e32 v42, v40, v40
	v_pk_add_f32 v[40:41], v[38:39], v[36:37] op_sel_hi:[1,0] neg_lo:[0,1] neg_hi:[0,1]
	v_fmac_f32_e32 v42, v37, v37
	v_pk_mul_f32 v[40:41], v[40:41], v[40:41]
	s_nop 0
	v_add_f32_e32 v37, v41, v42
	v_add_f32_e32 v37, v40, v37
	v_pk_add_f32 v[40:41], v[34:35], v[36:37] op_sel_hi:[1,0] neg_lo:[0,1] neg_hi:[0,1]
	s_nop 0
	v_pk_mul_f32 v[40:41], v[40:41], v[40:41]
	s_nop 0
	v_add_f32_e32 v37, v41, v37
	v_add_f32_e32 v37, v40, v37
	v_mov_b32_e32 v40, v37
	s_nop 1
	v_permlane32_swap_b32_e32 v40, v37
	s_waitcnt lgkmcnt(0)
	v_add_f32_e32 v37, v37, v40
	v_mov_b32_e32 v40, v37
	s_nop 1
	v_permlane16_swap_b32_e32 v40, v37
	s_waitcnt lgkmcnt(0)
	v_add_f32_e32 v37, v37, v40
	s_nop 1
	v_mov_b32_dpp v40, v37 row_ror:8 row_mask:0xf bank_mask:0xf
	s_waitcnt lgkmcnt(0)
	v_add_f32_e32 v37, v37, v40
	s_nop 1
	v_mov_b32_dpp v40, v37 row_shr:4 row_mask:0xf bank_mask:0xa
	v_mov_b32_dpp v40, v37 row_shl:4 row_mask:0xf bank_mask:0x5
	s_waitcnt lgkmcnt(0)
	v_add_f32_e32 v37, v37, v40
	s_nop 1
	v_mov_b32_dpp v40, v37 quad_perm:[2,3,0,1] row_mask:0xf bank_mask:0xf
	s_waitcnt lgkmcnt(0)
	v_add_f32_e32 v37, v37, v40
	s_nop 1
	v_mov_b32_dpp v40, v37 quad_perm:[1,0,3,2] row_mask:0xf bank_mask:0xf
	s_waitcnt lgkmcnt(0)
	v_add_f32_e32 v37, v37, v40
	v_fmamk_f32 v37, v37, 0x3a000000, v219
	v_mul_f32_e32 v40, 0x4b800000, v37
	v_cmp_gt_f32_e32 vcc, s33, v37
	s_nop 1
	v_cndmask_b32_e32 v37, v37, v40, vcc
	v_rsq_f32_e32 v37, v37
	s_nop 0
	v_mul_f32_e32 v40, 0x45800000, v37
	v_cndmask_b32_e32 v232, v37, v40, vcc
	ds_read_b128 v[40:43], v112 offset:12288
	ds_read_b128 v[44:47], v112 offset:4096
	ds_read_b128 v[48:51], v112 offset:4112
	ds_read_b128 v[52:55], v112 offset:12304
	v_mul_f32_e64 v233, v232, -v36
	v_fma_f32 v56, v56, v232, v233
	s_waitcnt lgkmcnt(2)
	v_fma_f32 v56, v56, v44, v40
	v_fma_f32 v40, v57, v232, v233
	v_fma_f32 v44, v89, v232, v233
	s_waitcnt lgkmcnt(0)
	v_fma_f32 v57, v40, v48, v52
	v_fma_f32 v40, v88, v232, v233
	v_fma_f32 v42, v44, v46, v42
	v_fma_f32 v44, v92, v232, v233
	v_fma_f32 v40, v40, v45, v41
	v_fma_f32 v41, v91, v232, v233
	v_fma_f32 v48, v44, v50, v54
	v_fma_f32 v44, v90, v232, v233
	v_fma_f32 v41, v41, v49, v53
	v_fmac_f32_e32 v43, v44, v47
	v_fma_f32 v44, v93, v232, v233
	v_fmac_f32_e32 v55, v44, v51
	v_cvt_pk_bf16_f32 v44, v56, v40
	v_cvt_pk_bf16_f32 v45, v42, v43
	v_cvt_pk_bf16_f32 v46, v57, v41
	v_cvt_pk_fp8_f32 v56, v56, v40
	v_cvt_pk_fp8_f32 v57, v57, v41
	v_cvt_pk_bf16_f32 v47, v48, v55
	global_store_dwordx4 v[84:85], v[44:47], off
	v_cvt_pk_fp8_f32 v56, v42, v43 op_sel:[0,0,1]
	v_cvt_pk_fp8_f32 v57, v48, v55 op_sel:[0,0,1]
	ds_read_b128 v[40:43], v112 offset:14336
	ds_read_b128 v[44:47], v112 offset:6144
	ds_read_b128 v[48:51], v112 offset:6160
	ds_read_b128 v[52:55], v112 offset:14352
	v_lshlrev_b64 v[36:37], 11, v[86:87]
	v_lshl_add_u64 v[86:87], v[78:79], 0, v[36:37]
	v_fma_f32 v36, v94, v232, v233
	s_waitcnt lgkmcnt(2)
	v_fma_f32 v36, v36, v44, v40
	v_fma_f32 v44, v96, v232, v233
	v_fma_f32 v37, v98, v232, v233
	v_fma_f32 v40, v95, v232, v233
	v_fma_f32 v42, v44, v46, v42
	v_fma_f32 v44, v100, v232, v233
	s_waitcnt lgkmcnt(0)
	v_fma_f32 v37, v37, v48, v52
	v_fma_f32 v40, v40, v45, v41
	v_fma_f32 v41, v99, v232, v233
	v_fma_f32 v48, v44, v50, v54
	v_fma_f32 v44, v97, v232, v233
	v_fma_f32 v41, v41, v49, v53
	v_fmac_f32_e32 v43, v44, v47
	v_fma_f32 v44, v101, v232, v233
	global_store_dwordx2 v[86:87], v[56:57], off
	v_fmac_f32_e32 v55, v44, v51
	v_cvt_pk_bf16_f32 v44, v36, v40
	v_cvt_pk_bf16_f32 v45, v42, v43
	v_cvt_pk_bf16_f32 v46, v37, v41
	v_cvt_pk_fp8_f32 v36, v36, v40
	v_cvt_pk_fp8_f32 v37, v37, v41
	v_cvt_pk_bf16_f32 v47, v48, v55
	global_store_dwordx4 v[84:85], v[44:47], off offset:1024
	v_cvt_pk_fp8_f32 v36, v42, v43 op_sel:[0,0,1]
	v_cvt_pk_fp8_f32 v37, v48, v55 op_sel:[0,0,1]
	ds_read_b128 v[40:43], v112 offset:16384
	ds_read_b128 v[44:47], v112 offset:8192
	ds_read_b128 v[48:51], v112 offset:8208
	ds_read_b128 v[52:55], v112 offset:16400
	v_fma_f32 v35, v35, v232, v233
	global_store_dwordx2 v[86:87], v[36:37], off offset:512
	v_fma_f32 v36, v122, v232, v233
	s_waitcnt lgkmcnt(2)
	v_fma_f32 v36, v36, v44, v40
	v_fma_f32 v44, v222, v232, v233
	v_fma_f32 v37, v224, v232, v233
	v_fma_f32 v40, v123, v232, v233
	v_fma_f32 v42, v44, v46, v42
	v_fma_f32 v44, v226, v232, v233
	s_waitcnt lgkmcnt(0)
	v_fma_f32 v37, v37, v48, v52
	v_fma_f32 v40, v40, v45, v41
	v_fma_f32 v41, v225, v232, v233
	v_fma_f32 v48, v44, v50, v54
	v_fma_f32 v44, v223, v232, v233
	v_fma_f32 v41, v41, v49, v53
	v_fmac_f32_e32 v43, v44, v47
	v_fma_f32 v44, v227, v232, v233
	v_fmac_f32_e32 v55, v44, v51
	v_cvt_pk_bf16_f32 v44, v36, v40
	v_cvt_pk_bf16_f32 v45, v42, v43
	v_cvt_pk_bf16_f32 v46, v37, v41
	v_cvt_pk_fp8_f32 v36, v36, v40
	v_cvt_pk_fp8_f32 v37, v37, v41
	v_cvt_pk_bf16_f32 v47, v48, v55
	global_store_dwordx4 v[84:85], v[44:47], off offset:2048
	v_cvt_pk_fp8_f32 v36, v42, v43 op_sel:[0,0,1]
	v_cvt_pk_fp8_f32 v37, v48, v55 op_sel:[0,0,1]
	ds_read_b128 v[40:43], v112 offset:18432
	ds_read_b128 v[44:47], v112 offset:10240
	ds_read_b128 v[48:51], v112 offset:10256
	ds_read_b128 v[52:55], v112 offset:18448
	global_store_dwordx2 v[86:87], v[36:37], off offset:1024
	v_fma_f32 v36, v228, v232, v233
	s_waitcnt lgkmcnt(2)
	v_fma_f32 v56, v36, v44, v40
	v_fma_f32 v36, v39, v232, v233
	s_waitcnt lgkmcnt(0)
	v_fma_f32 v57, v36, v48, v52
	v_fma_f32 v36, v229, v232, v233
	v_fma_f32 v39, v36, v45, v41
	v_fma_f32 v36, v38, v232, v233
	v_fma_f32 v40, v36, v49, v53
	v_fma_f32 v36, v230, v232, v233
	v_fma_f32 v41, v36, v46, v42
	v_fma_f32 v36, v231, v232, v233
	v_fmac_f32_e32 v43, v36, v47
	v_cvt_pk_bf16_f32 v36, v56, v39
	v_cvt_pk_bf16_f32 v37, v41, v43
	v_cvt_pk_bf16_f32 v38, v57, v40
	v_cvt_pk_fp8_f32 v56, v56, v39
	v_cvt_pk_fp8_f32 v57, v57, v40
	v_fmac_f32_e32 v233, v34, v232
	v_fma_f32 v35, v35, v50, v54
	v_fmac_f32_e32 v55, v233, v51
	v_cvt_pk_fp8_f32 v56, v41, v43 op_sel:[0,0,1]
	v_cvt_pk_fp8_f32 v57, v35, v55 op_sel:[0,0,1]
	v_cvt_pk_bf16_f32 v39, v35, v55
	global_store_dwordx4 v[84:85], v[36:39], off offset:3072
	global_store_dwordx2 v[86:87], v[56:57], off offset:1536
	s_waitcnt vmcnt(23)
	v_lshlrev_b32_e32 v40, 16, v30
	v_and_b32_e32 v42, 0xffff0000, v30
	s_waitcnt vmcnt(20)
	v_lshlrev_b32_e32 v90, 16, v18
	v_and_b32_e32 v91, 0xffff0000, v18
	v_add_f32_e32 v18, 0, v40
	v_lshlrev_b32_e32 v43, 16, v31
	v_add_f32_e32 v18, v18, v42
	v_and_b32_e32 v44, 0xffff0000, v31
	v_add_f32_e32 v18, v18, v43
	v_lshlrev_b32_e32 v41, 16, v32
	v_add_f32_e32 v18, v18, v44
	v_and_b32_e32 v45, 0xffff0000, v32
	v_add_f32_e32 v18, v18, v41
	v_lshlrev_b32_e32 v46, 16, v33
	v_add_f32_e32 v18, v18, v45
	v_and_b32_e32 v47, 0xffff0000, v33
	v_add_f32_e32 v18, v18, v46
	v_lshlrev_b32_e32 v48, 16, v26
	v_add_f32_e32 v18, v18, v47
	v_and_b32_e32 v49, 0xffff0000, v26
	v_add_f32_e32 v18, v18, v48
	v_lshlrev_b32_e32 v50, 16, v27
	v_add_f32_e32 v18, v18, v49
	v_and_b32_e32 v51, 0xffff0000, v27
	v_add_f32_e32 v18, v18, v50
	v_lshlrev_b32_e32 v52, 16, v28
	v_add_f32_e32 v18, v18, v51
	v_and_b32_e32 v53, 0xffff0000, v28
	v_add_f32_e32 v18, v18, v52
	v_lshlrev_b32_e32 v54, 16, v29
	v_add_f32_e32 v18, v18, v53
	v_and_b32_e32 v55, 0xffff0000, v29
	v_add_f32_e32 v18, v18, v54
	v_lshlrev_b32_e32 v56, 16, v22
	v_add_f32_e32 v18, v18, v55
	v_and_b32_e32 v57, 0xffff0000, v22
	v_add_f32_e32 v18, v18, v56
	v_lshlrev_b32_e32 v84, 16, v23
	v_add_f32_e32 v18, v18, v57
	v_and_b32_e32 v85, 0xffff0000, v23
	v_add_f32_e32 v18, v18, v84
	v_lshlrev_b32_e32 v86, 16, v24
	v_add_f32_e32 v18, v18, v85
	v_and_b32_e32 v87, 0xffff0000, v24
	v_add_f32_e32 v18, v18, v86
	v_lshlrev_b32_e32 v88, 16, v25
	v_add_f32_e32 v18, v18, v87
	v_and_b32_e32 v89, 0xffff0000, v25
	v_add_f32_e32 v18, v18, v88
	v_add_f32_e32 v18, v18, v89
	v_add_f32_e32 v18, v18, v90
	v_lshlrev_b32_e32 v92, 16, v19
	v_add_f32_e32 v18, v18, v91
	v_and_b32_e32 v93, 0xffff0000, v19
	v_add_f32_e32 v18, v18, v92
	v_add_f32_e32 v24, v18, v93
	v_lshlrev_b32_e32 v23, 16, v20
	v_and_b32_e32 v22, 0xffff0000, v20
	v_add_f32_e32 v20, v24, v23
	v_lshlrev_b32_e32 v19, 16, v21
	v_add_f32_e32 v20, v20, v22
	v_and_b32_e32 v18, 0xffff0000, v21
	v_add_f32_e32 v20, v20, v19
	v_add_f32_e32 v20, v20, v18
	v_mov_b32_e32 v21, v20
	s_nop 1
	v_permlane32_swap_b32_e32 v21, v20
	s_waitcnt lgkmcnt(0)
	v_add_f32_e32 v20, v20, v21
	v_mov_b32_e32 v21, v20
	s_nop 1
	v_permlane16_swap_b32_e32 v21, v20
	s_waitcnt lgkmcnt(0)
	v_add_f32_e32 v20, v20, v21
	s_nop 1
	v_mov_b32_dpp v21, v20 row_ror:8 row_mask:0xf bank_mask:0xf
	s_waitcnt lgkmcnt(0)
	v_add_f32_e32 v20, v20, v21
	s_nop 1
	v_mov_b32_dpp v21, v20 row_shr:4 row_mask:0xf bank_mask:0xa
	v_mov_b32_dpp v21, v20 row_shl:4 row_mask:0xf bank_mask:0x5
	s_waitcnt lgkmcnt(0)
	v_add_f32_e32 v20, v20, v21
	s_nop 1
	v_mov_b32_dpp v21, v20 quad_perm:[2,3,0,1] row_mask:0xf bank_mask:0xf
	s_waitcnt lgkmcnt(0)
	v_add_f32_e32 v20, v20, v21
	s_nop 1
	v_mov_b32_dpp v21, v20 quad_perm:[1,0,3,2] row_mask:0xf bank_mask:0xf
	s_waitcnt lgkmcnt(0)
	v_add_f32_e32 v21, v20, v21
	v_fmamk_f32 v25, v21, 0xba000000, v42
	v_fmamk_f32 v24, v21, 0xba000000, v40
	v_mul_f32_e32 v26, v25, v25
	v_fmac_f32_e32 v26, v24, v24
	v_fmamk_f32 v24, v21, 0xba000000, v43
	v_fmac_f32_e32 v26, v24, v24
	v_fmamk_f32 v24, v21, 0xba000000, v44
	v_fmac_f32_e32 v26, v24, v24
	v_fmamk_f32 v24, v21, 0xba000000, v41
	v_fmac_f32_e32 v26, v24, v24
	v_fmamk_f32 v24, v21, 0xba000000, v45
	v_fmac_f32_e32 v26, v24, v24
	v_fmamk_f32 v24, v21, 0xba000000, v46
	v_fmac_f32_e32 v26, v24, v24
	v_fmamk_f32 v24, v21, 0xba000000, v47
	v_fmac_f32_e32 v26, v24, v24
	v_fmamk_f32 v24, v21, 0xba000000, v48
	v_fmac_f32_e32 v26, v24, v24
	v_fmamk_f32 v24, v21, 0xba000000, v49
	v_fmac_f32_e32 v26, v24, v24
	v_fmamk_f32 v24, v21, 0xba000000, v50
	v_fmac_f32_e32 v26, v24, v24
	v_fmamk_f32 v24, v21, 0xba000000, v51
	v_fmac_f32_e32 v26, v24, v24
	v_fmamk_f32 v24, v21, 0xba000000, v52
	v_fmac_f32_e32 v26, v24, v24
	v_fmamk_f32 v24, v21, 0xba000000, v53
	v_fmac_f32_e32 v26, v24, v24
	v_fmamk_f32 v24, v21, 0xba000000, v54
	v_fmac_f32_e32 v26, v24, v24
	v_fmamk_f32 v24, v21, 0xba000000, v55
	v_fmac_f32_e32 v26, v24, v24
	v_fmamk_f32 v24, v21, 0xba000000, v56
	v_fmac_f32_e32 v26, v24, v24
	v_fmamk_f32 v24, v21, 0xba000000, v57
	v_fmac_f32_e32 v26, v24, v24
	v_fmamk_f32 v24, v21, 0xba000000, v84
	v_fmac_f32_e32 v26, v24, v24
	v_fmamk_f32 v24, v21, 0xba000000, v85
	v_fmac_f32_e32 v26, v24, v24
	v_fmamk_f32 v24, v21, 0xba000000, v86
	v_fmac_f32_e32 v26, v24, v24
	v_fmamk_f32 v24, v21, 0xba000000, v87
	v_fmac_f32_e32 v26, v24, v24
	v_fmamk_f32 v24, v21, 0xba000000, v88
	v_fmac_f32_e32 v26, v24, v24
	v_fmamk_f32 v24, v21, 0xba000000, v89
	v_fmac_f32_e32 v26, v24, v24
	v_fmamk_f32 v24, v21, 0xba000000, v90
	v_fmac_f32_e32 v26, v24, v24
	v_fmamk_f32 v24, v21, 0xba000000, v91
	v_mul_f32_e32 v20, 0x3a000000, v21
	v_fmac_f32_e32 v26, v24, v24
	v_fmamk_f32 v24, v21, 0xba000000, v92
	v_fmamk_f32 v21, v21, 0xba000000, v93
	v_fmac_f32_e32 v26, v24, v24
	v_pk_add_f32 v[24:25], v[22:23], v[20:21] op_sel_hi:[1,0] neg_lo:[0,1] neg_hi:[0,1]
	v_fmac_f32_e32 v26, v21, v21
	v_pk_mul_f32 v[24:25], v[24:25], v[24:25]
	s_nop 0
	v_add_f32_e32 v21, v25, v26
	v_add_f32_e32 v21, v24, v21
	v_pk_add_f32 v[24:25], v[18:19], v[20:21] op_sel_hi:[1,0] neg_lo:[0,1] neg_hi:[0,1]
	s_nop 0
	v_pk_mul_f32 v[24:25], v[24:25], v[24:25]
	s_nop 0
	v_add_f32_e32 v21, v25, v21
	v_add_f32_e32 v21, v24, v21
	v_mov_b32_e32 v24, v21
	s_nop 1
	v_permlane32_swap_b32_e32 v24, v21
	s_waitcnt lgkmcnt(0)
	v_add_f32_e32 v21, v21, v24
	v_mov_b32_e32 v24, v21
	s_nop 1
	v_permlane16_swap_b32_e32 v24, v21
	s_waitcnt lgkmcnt(0)
	v_add_f32_e32 v21, v21, v24
	s_nop 1
	v_mov_b32_dpp v24, v21 row_ror:8 row_mask:0xf bank_mask:0xf
	s_waitcnt lgkmcnt(0)
	v_add_f32_e32 v21, v21, v24
	s_nop 1
	v_mov_b32_dpp v24, v21 row_shr:4 row_mask:0xf bank_mask:0xa
	v_mov_b32_dpp v24, v21 row_shl:4 row_mask:0xf bank_mask:0x5
	s_waitcnt lgkmcnt(0)
	v_add_f32_e32 v21, v21, v24
	s_nop 1
	v_mov_b32_dpp v24, v21 quad_perm:[2,3,0,1] row_mask:0xf bank_mask:0xf
	s_waitcnt lgkmcnt(0)
	v_add_f32_e32 v21, v21, v24
	s_nop 1
	v_mov_b32_dpp v24, v21 quad_perm:[1,0,3,2] row_mask:0xf bank_mask:0xf
	s_waitcnt lgkmcnt(0)
	v_add_f32_e32 v21, v21, v24
	v_fmamk_f32 v21, v21, 0x3a000000, v219
	v_mul_f32_e32 v24, 0x4b800000, v21
	v_cmp_gt_f32_e32 vcc, s33, v21
	s_nop 1
	v_cndmask_b32_e32 v21, v21, v24, vcc
	v_rsq_f32_e32 v21, v21
	s_nop 0
	v_mul_f32_e32 v24, 0x45800000, v21
	v_cndmask_b32_e32 v94, v21, v24, vcc
	ds_read_b128 v[24:27], v112 offset:12288
	ds_read_b128 v[28:31], v112 offset:4096
	ds_read_b128 v[32:35], v112 offset:4112
	ds_read_b128 v[36:39], v112 offset:12304
	v_mul_f32_e64 v95, v94, -v20
	v_fma_f32 v40, v40, v94, v95
	s_waitcnt lgkmcnt(2)
	v_fma_f32 v40, v40, v28, v24
	v_fma_f32 v24, v41, v94, v95
	v_fma_f32 v28, v43, v94, v95
	s_waitcnt lgkmcnt(0)
	v_fma_f32 v41, v24, v32, v36
	v_fma_f32 v24, v42, v94, v95
	v_fma_f32 v26, v28, v30, v26
	v_fma_f32 v28, v46, v94, v95
	v_fma_f32 v24, v24, v29, v25
	v_fma_f32 v25, v45, v94, v95
	v_fma_f32 v32, v28, v34, v38
	v_fma_f32 v28, v44, v94, v95
	v_fma_f32 v25, v25, v33, v37
	v_fmac_f32_e32 v27, v28, v31
	v_fma_f32 v28, v47, v94, v95
	v_fmac_f32_e32 v39, v28, v35
	v_cvt_pk_bf16_f32 v28, v40, v24
	v_cvt_pk_bf16_f32 v29, v26, v27
	v_cvt_pk_bf16_f32 v30, v41, v25
	v_cvt_pk_fp8_f32 v40, v40, v24
	v_cvt_pk_fp8_f32 v41, v41, v25
	v_lshl_add_u64 v[42:43], v[76:77], 0, v[62:63]
	v_cvt_pk_bf16_f32 v31, v32, v39
	global_store_dwordx4 v[42:43], v[28:31], off
	v_cvt_pk_fp8_f32 v40, v26, v27 op_sel:[0,0,1]
	v_cvt_pk_fp8_f32 v41, v32, v39 op_sel:[0,0,1]
	ds_read_b128 v[24:27], v112 offset:14336
	ds_read_b128 v[28:31], v112 offset:6144
	ds_read_b128 v[32:35], v112 offset:6160
	ds_read_b128 v[36:39], v112 offset:14352
	v_lshlrev_b64 v[20:21], 11, v[64:65]
	v_lshl_add_u64 v[44:45], v[78:79], 0, v[20:21]
	v_fma_f32 v20, v48, v94, v95
	s_waitcnt lgkmcnt(2)
	v_fma_f32 v20, v20, v28, v24
	v_fma_f32 v28, v50, v94, v95
	v_fma_f32 v21, v52, v94, v95
	v_fma_f32 v24, v49, v94, v95
	v_fma_f32 v26, v28, v30, v26
	v_fma_f32 v28, v54, v94, v95
	s_waitcnt lgkmcnt(0)
	v_fma_f32 v21, v21, v32, v36
	v_fma_f32 v24, v24, v29, v25
	v_fma_f32 v25, v53, v94, v95
	v_fma_f32 v32, v28, v34, v38
	v_fma_f32 v28, v51, v94, v95
	v_fma_f32 v25, v25, v33, v37
	v_fmac_f32_e32 v27, v28, v31
	v_fma_f32 v28, v55, v94, v95
	global_store_dwordx2 v[44:45], v[40:41], off
	v_fmac_f32_e32 v39, v28, v35
	v_cvt_pk_bf16_f32 v28, v20, v24
	v_cvt_pk_bf16_f32 v29, v26, v27
	v_cvt_pk_bf16_f32 v30, v21, v25
	v_cvt_pk_fp8_f32 v20, v20, v24
	v_cvt_pk_fp8_f32 v21, v21, v25
	v_cvt_pk_bf16_f32 v31, v32, v39
	global_store_dwordx4 v[42:43], v[28:31], off offset:1024
	v_cvt_pk_fp8_f32 v20, v26, v27 op_sel:[0,0,1]
	v_cvt_pk_fp8_f32 v21, v32, v39 op_sel:[0,0,1]
	ds_read_b128 v[24:27], v112 offset:16384
	ds_read_b128 v[28:31], v112 offset:8192
	ds_read_b128 v[32:35], v112 offset:8208
	ds_read_b128 v[36:39], v112 offset:16400
	v_fma_f32 v19, v19, v94, v95
	global_store_dwordx2 v[44:45], v[20:21], off offset:512
	v_fma_f32 v20, v56, v94, v95
	s_waitcnt lgkmcnt(2)
	v_fma_f32 v20, v20, v28, v24
	v_fma_f32 v28, v84, v94, v95
	v_fma_f32 v21, v86, v94, v95
	v_fma_f32 v24, v57, v94, v95
	v_fma_f32 v26, v28, v30, v26
	v_fma_f32 v28, v88, v94, v95
	s_waitcnt lgkmcnt(0)
	v_fma_f32 v21, v21, v32, v36
	v_fma_f32 v24, v24, v29, v25
	v_fma_f32 v25, v87, v94, v95
	v_fma_f32 v32, v28, v34, v38
	v_fma_f32 v28, v85, v94, v95
	v_fma_f32 v25, v25, v33, v37
	v_fmac_f32_e32 v27, v28, v31
	v_fma_f32 v28, v89, v94, v95
	v_fmac_f32_e32 v39, v28, v35
	v_cvt_pk_bf16_f32 v28, v20, v24
	v_cvt_pk_bf16_f32 v29, v26, v27
	v_cvt_pk_bf16_f32 v30, v21, v25
	v_cvt_pk_fp8_f32 v20, v20, v24
	v_cvt_pk_fp8_f32 v21, v21, v25
	v_cvt_pk_bf16_f32 v31, v32, v39
	global_store_dwordx4 v[42:43], v[28:31], off offset:2048
	v_cvt_pk_fp8_f32 v20, v26, v27 op_sel:[0,0,1]
	v_cvt_pk_fp8_f32 v21, v32, v39 op_sel:[0,0,1]
	ds_read_b128 v[24:27], v112 offset:18432
	ds_read_b128 v[28:31], v112 offset:10240
	ds_read_b128 v[32:35], v112 offset:10256
	ds_read_b128 v[36:39], v112 offset:18448
	global_store_dwordx2 v[44:45], v[20:21], off offset:1024
	v_fma_f32 v20, v90, v94, v95
	s_waitcnt lgkmcnt(2)
	v_fma_f32 v40, v20, v28, v24
	v_fma_f32 v20, v23, v94, v95
	s_waitcnt lgkmcnt(0)
	v_fma_f32 v41, v20, v32, v36
	v_fma_f32 v20, v91, v94, v95
	v_fma_f32 v23, v20, v29, v25
	v_fma_f32 v20, v22, v94, v95
	v_fma_f32 v24, v20, v33, v37
	v_fma_f32 v20, v92, v94, v95
	v_fma_f32 v25, v20, v30, v26
	v_fma_f32 v20, v93, v94, v95
	v_fmac_f32_e32 v27, v20, v31
	v_cvt_pk_bf16_f32 v20, v40, v23
	v_cvt_pk_bf16_f32 v21, v25, v27
	v_cvt_pk_bf16_f32 v22, v41, v24
	v_cvt_pk_fp8_f32 v40, v40, v23
	v_cvt_pk_fp8_f32 v41, v41, v24
	v_fmac_f32_e32 v95, v18, v94
	v_fma_f32 v19, v19, v34, v38
	v_fmac_f32_e32 v39, v95, v35
	v_cvt_pk_fp8_f32 v40, v25, v27 op_sel:[0,0,1]
	v_cvt_pk_fp8_f32 v41, v19, v39 op_sel:[0,0,1]
	v_cvt_pk_bf16_f32 v23, v19, v39
	global_store_dwordx4 v[42:43], v[20:23], off offset:3072
	global_store_dwordx2 v[44:45], v[40:41], off offset:1536
	s_waitcnt vmcnt(27)
	v_lshlrev_b32_e32 v24, 16, v14
	v_and_b32_e32 v26, 0xffff0000, v14
	s_waitcnt vmcnt(24)
	v_lshlrev_b32_e32 v48, 16, v2
	v_and_b32_e32 v49, 0xffff0000, v2
	v_add_f32_e32 v2, 0, v24
	v_lshlrev_b32_e32 v27, 16, v15
	v_add_f32_e32 v2, v2, v26
	v_and_b32_e32 v28, 0xffff0000, v15
	v_add_f32_e32 v2, v2, v27
	v_lshlrev_b32_e32 v25, 16, v16
	v_add_f32_e32 v2, v2, v28
	v_and_b32_e32 v29, 0xffff0000, v16
	v_add_f32_e32 v2, v2, v25
	v_lshlrev_b32_e32 v30, 16, v17
	v_add_f32_e32 v2, v2, v29
	v_and_b32_e32 v31, 0xffff0000, v17
	v_add_f32_e32 v2, v2, v30
	v_lshlrev_b32_e32 v32, 16, v10
	v_add_f32_e32 v2, v2, v31
	v_and_b32_e32 v33, 0xffff0000, v10
	v_add_f32_e32 v2, v2, v32
	v_lshlrev_b32_e32 v34, 16, v11
	v_add_f32_e32 v2, v2, v33
	v_and_b32_e32 v35, 0xffff0000, v11
	v_add_f32_e32 v2, v2, v34
	v_lshlrev_b32_e32 v36, 16, v12
	v_add_f32_e32 v2, v2, v35
	v_and_b32_e32 v37, 0xffff0000, v12
	v_add_f32_e32 v2, v2, v36
	v_lshlrev_b32_e32 v38, 16, v13
	v_add_f32_e32 v2, v2, v37
	v_and_b32_e32 v39, 0xffff0000, v13
	v_add_f32_e32 v2, v2, v38
	v_lshlrev_b32_e32 v40, 16, v6
	v_add_f32_e32 v2, v2, v39
	v_and_b32_e32 v41, 0xffff0000, v6
	v_add_f32_e32 v2, v2, v40
	v_lshlrev_b32_e32 v42, 16, v7
	v_add_f32_e32 v2, v2, v41
	v_and_b32_e32 v43, 0xffff0000, v7
	v_add_f32_e32 v2, v2, v42
	v_lshlrev_b32_e32 v44, 16, v8
	v_add_f32_e32 v2, v2, v43
	v_and_b32_e32 v45, 0xffff0000, v8
	v_add_f32_e32 v2, v2, v44
	v_lshlrev_b32_e32 v46, 16, v9
	v_add_f32_e32 v2, v2, v45
	v_and_b32_e32 v47, 0xffff0000, v9
	v_add_f32_e32 v2, v2, v46
	v_add_f32_e32 v2, v2, v47
	v_add_f32_e32 v2, v2, v48
	v_lshlrev_b32_e32 v50, 16, v3
	v_add_f32_e32 v2, v2, v49
	v_and_b32_e32 v51, 0xffff0000, v3
	v_add_f32_e32 v2, v2, v50
	v_add_f32_e32 v8, v2, v51
	v_lshlrev_b32_e32 v7, 16, v4
	v_and_b32_e32 v6, 0xffff0000, v4
	v_add_f32_e32 v4, v8, v7
	v_lshlrev_b32_e32 v3, 16, v5
	v_add_f32_e32 v4, v4, v6
	v_and_b32_e32 v2, 0xffff0000, v5
	v_add_f32_e32 v4, v4, v3
	v_add_f32_e32 v4, v4, v2
	v_mov_b32_e32 v5, v4
	s_nop 1
	v_permlane32_swap_b32_e32 v5, v4
	s_waitcnt lgkmcnt(0)
	v_add_f32_e32 v4, v4, v5
	v_mov_b32_e32 v5, v4
	s_nop 1
	v_permlane16_swap_b32_e32 v5, v4
	s_waitcnt lgkmcnt(0)
	v_add_f32_e32 v4, v4, v5
	s_nop 1
	v_mov_b32_dpp v5, v4 row_ror:8 row_mask:0xf bank_mask:0xf
	s_waitcnt lgkmcnt(0)
	v_add_f32_e32 v4, v4, v5
	s_nop 1
	v_mov_b32_dpp v5, v4 row_shr:4 row_mask:0xf bank_mask:0xa
	v_mov_b32_dpp v5, v4 row_shl:4 row_mask:0xf bank_mask:0x5
	s_waitcnt lgkmcnt(0)
	v_add_f32_e32 v4, v4, v5
	s_nop 1
	v_mov_b32_dpp v5, v4 quad_perm:[2,3,0,1] row_mask:0xf bank_mask:0xf
	s_waitcnt lgkmcnt(0)
	v_add_f32_e32 v4, v4, v5
	s_nop 1
	v_mov_b32_dpp v5, v4 quad_perm:[1,0,3,2] row_mask:0xf bank_mask:0xf
	s_waitcnt lgkmcnt(0)
	v_add_f32_e32 v5, v4, v5
	v_fmamk_f32 v9, v5, 0xba000000, v26
	v_fmamk_f32 v8, v5, 0xba000000, v24
	v_mul_f32_e32 v10, v9, v9
	v_fmac_f32_e32 v10, v8, v8
	v_fmamk_f32 v8, v5, 0xba000000, v27
	v_fmac_f32_e32 v10, v8, v8
	v_fmamk_f32 v8, v5, 0xba000000, v28
	v_fmac_f32_e32 v10, v8, v8
	v_fmamk_f32 v8, v5, 0xba000000, v25
	v_fmac_f32_e32 v10, v8, v8
	v_fmamk_f32 v8, v5, 0xba000000, v29
	v_fmac_f32_e32 v10, v8, v8
	v_fmamk_f32 v8, v5, 0xba000000, v30
	v_fmac_f32_e32 v10, v8, v8
	v_fmamk_f32 v8, v5, 0xba000000, v31
	v_fmac_f32_e32 v10, v8, v8
	v_fmamk_f32 v8, v5, 0xba000000, v32
	v_fmac_f32_e32 v10, v8, v8
	v_fmamk_f32 v8, v5, 0xba000000, v33
	v_fmac_f32_e32 v10, v8, v8
	v_fmamk_f32 v8, v5, 0xba000000, v34
	v_fmac_f32_e32 v10, v8, v8
	v_fmamk_f32 v8, v5, 0xba000000, v35
	v_fmac_f32_e32 v10, v8, v8
	v_fmamk_f32 v8, v5, 0xba000000, v36
	v_fmac_f32_e32 v10, v8, v8
	v_fmamk_f32 v8, v5, 0xba000000, v37
	v_fmac_f32_e32 v10, v8, v8
	v_fmamk_f32 v8, v5, 0xba000000, v38
	v_fmac_f32_e32 v10, v8, v8
	v_fmamk_f32 v8, v5, 0xba000000, v39
	v_fmac_f32_e32 v10, v8, v8
	v_fmamk_f32 v8, v5, 0xba000000, v40
	v_fmac_f32_e32 v10, v8, v8
	v_fmamk_f32 v8, v5, 0xba000000, v41
	v_fmac_f32_e32 v10, v8, v8
	v_fmamk_f32 v8, v5, 0xba000000, v42
	v_fmac_f32_e32 v10, v8, v8
	v_fmamk_f32 v8, v5, 0xba000000, v43
	v_fmac_f32_e32 v10, v8, v8
	v_fmamk_f32 v8, v5, 0xba000000, v44
	v_fmac_f32_e32 v10, v8, v8
	v_fmamk_f32 v8, v5, 0xba000000, v45
	v_fmac_f32_e32 v10, v8, v8
	v_fmamk_f32 v8, v5, 0xba000000, v46
	v_fmac_f32_e32 v10, v8, v8
	v_fmamk_f32 v8, v5, 0xba000000, v47
	v_fmac_f32_e32 v10, v8, v8
	v_fmamk_f32 v8, v5, 0xba000000, v48
	v_fmac_f32_e32 v10, v8, v8
	v_fmamk_f32 v8, v5, 0xba000000, v49
	v_mul_f32_e32 v4, 0x3a000000, v5
	v_fmac_f32_e32 v10, v8, v8
	v_fmamk_f32 v8, v5, 0xba000000, v50
	v_fmamk_f32 v5, v5, 0xba000000, v51
	v_fmac_f32_e32 v10, v8, v8
	v_pk_add_f32 v[8:9], v[6:7], v[4:5] op_sel_hi:[1,0] neg_lo:[0,1] neg_hi:[0,1]
	v_fmac_f32_e32 v10, v5, v5
	v_pk_mul_f32 v[8:9], v[8:9], v[8:9]
	s_nop 0
	v_add_f32_e32 v5, v9, v10
	v_add_f32_e32 v5, v8, v5
	v_pk_add_f32 v[8:9], v[2:3], v[4:5] op_sel_hi:[1,0] neg_lo:[0,1] neg_hi:[0,1]
	s_nop 0
	v_pk_mul_f32 v[8:9], v[8:9], v[8:9]
	s_nop 0
	v_add_f32_e32 v5, v9, v5
	v_add_f32_e32 v5, v8, v5
	v_mov_b32_e32 v8, v5
	s_nop 1
	v_permlane32_swap_b32_e32 v8, v5
	s_waitcnt lgkmcnt(0)
	v_add_f32_e32 v5, v5, v8
	v_mov_b32_e32 v8, v5
	s_nop 1
	v_permlane16_swap_b32_e32 v8, v5
	s_waitcnt lgkmcnt(0)
	v_add_f32_e32 v5, v5, v8
	s_nop 1
	v_mov_b32_dpp v8, v5 row_ror:8 row_mask:0xf bank_mask:0xf
	s_waitcnt lgkmcnt(0)
	v_add_f32_e32 v5, v5, v8
	s_nop 1
	v_mov_b32_dpp v8, v5 row_shr:4 row_mask:0xf bank_mask:0xa
	v_mov_b32_dpp v8, v5 row_shl:4 row_mask:0xf bank_mask:0x5
	s_waitcnt lgkmcnt(0)
	v_add_f32_e32 v5, v5, v8
	s_nop 1
	v_mov_b32_dpp v8, v5 quad_perm:[2,3,0,1] row_mask:0xf bank_mask:0xf
	s_waitcnt lgkmcnt(0)
	v_add_f32_e32 v5, v5, v8
	s_nop 1
	v_mov_b32_dpp v8, v5 quad_perm:[1,0,3,2] row_mask:0xf bank_mask:0xf
	s_waitcnt lgkmcnt(0)
	v_add_f32_e32 v5, v5, v8
	v_fmamk_f32 v5, v5, 0x3a000000, v219
	v_mul_f32_e32 v8, 0x4b800000, v5
	v_cmp_gt_f32_e32 vcc, s33, v5
	s_nop 1
	v_cndmask_b32_e32 v5, v5, v8, vcc
	v_rsq_f32_e32 v5, v5
	s_nop 0
	v_mul_f32_e32 v8, 0x45800000, v5
	v_cndmask_b32_e32 v52, v5, v8, vcc
	ds_read_b128 v[8:11], v112 offset:12288
	ds_read_b128 v[12:15], v112 offset:4096
	ds_read_b128 v[16:19], v112 offset:4112
	ds_read_b128 v[20:23], v112 offset:12304
	v_mul_f32_e64 v53, v52, -v4
	v_fma_f32 v24, v24, v52, v53
	s_waitcnt lgkmcnt(2)
	v_fma_f32 v24, v24, v12, v8
	v_fma_f32 v8, v25, v52, v53
	v_fma_f32 v12, v27, v52, v53
	s_waitcnt lgkmcnt(0)
	v_fma_f32 v25, v8, v16, v20
	v_fma_f32 v8, v26, v52, v53
	v_fma_f32 v10, v12, v14, v10
	v_fma_f32 v12, v30, v52, v53
	v_fma_f32 v8, v8, v13, v9
	v_fma_f32 v9, v29, v52, v53
	v_fma_f32 v16, v12, v18, v22
	v_fma_f32 v12, v28, v52, v53
	v_fma_f32 v9, v9, v17, v21
	v_fmac_f32_e32 v11, v12, v15
	v_fma_f32 v12, v31, v52, v53
	v_fmac_f32_e32 v23, v12, v19
	v_cvt_pk_bf16_f32 v12, v24, v8
	v_cvt_pk_bf16_f32 v13, v10, v11
	v_cvt_pk_bf16_f32 v14, v25, v9
	v_cvt_pk_fp8_f32 v24, v24, v8
	v_cvt_pk_fp8_f32 v25, v25, v9
	v_lshl_add_u64 v[26:27], v[76:77], 0, v[58:59]
	v_cvt_pk_bf16_f32 v15, v16, v23
	global_store_dwordx4 v[26:27], v[12:15], off
	v_cvt_pk_fp8_f32 v24, v10, v11 op_sel:[0,0,1]
	v_cvt_pk_fp8_f32 v25, v16, v23 op_sel:[0,0,1]
	ds_read_b128 v[8:11], v112 offset:14336
	ds_read_b128 v[12:15], v112 offset:6144
	ds_read_b128 v[16:19], v112 offset:6160
	ds_read_b128 v[20:23], v112 offset:14352
	v_lshlrev_b64 v[4:5], 11, v[60:61]
	v_lshl_add_u64 v[28:29], v[78:79], 0, v[4:5]
	v_fma_f32 v4, v32, v52, v53
	s_waitcnt lgkmcnt(2)
	v_fma_f32 v4, v4, v12, v8
	v_fma_f32 v12, v34, v52, v53
	v_fma_f32 v5, v36, v52, v53
	v_fma_f32 v8, v33, v52, v53
	v_fma_f32 v10, v12, v14, v10
	v_fma_f32 v12, v38, v52, v53
	s_waitcnt lgkmcnt(0)
	v_fma_f32 v5, v5, v16, v20
	v_fma_f32 v8, v8, v13, v9
	v_fma_f32 v9, v37, v52, v53
	v_fma_f32 v16, v12, v18, v22
	v_fma_f32 v12, v35, v52, v53
	v_fma_f32 v9, v9, v17, v21
	v_fmac_f32_e32 v11, v12, v15
	v_fma_f32 v12, v39, v52, v53
	global_store_dwordx2 v[28:29], v[24:25], off
	v_fmac_f32_e32 v23, v12, v19
	v_cvt_pk_bf16_f32 v12, v4, v8
	v_cvt_pk_bf16_f32 v13, v10, v11
	v_cvt_pk_bf16_f32 v14, v5, v9
	v_cvt_pk_fp8_f32 v4, v4, v8
	v_cvt_pk_fp8_f32 v5, v5, v9
	v_cvt_pk_bf16_f32 v15, v16, v23
	global_store_dwordx4 v[26:27], v[12:15], off offset:1024
	v_cvt_pk_fp8_f32 v4, v10, v11 op_sel:[0,0,1]
	v_cvt_pk_fp8_f32 v5, v16, v23 op_sel:[0,0,1]
	ds_read_b128 v[8:11], v112 offset:16384
	ds_read_b128 v[12:15], v112 offset:8192
	ds_read_b128 v[16:19], v112 offset:8208
	ds_read_b128 v[20:23], v112 offset:16400
	v_fma_f32 v3, v3, v52, v53
	global_store_dwordx2 v[28:29], v[4:5], off offset:512
	v_fma_f32 v4, v40, v52, v53
	s_waitcnt lgkmcnt(2)
	v_fma_f32 v4, v4, v12, v8
	v_fma_f32 v12, v42, v52, v53
	v_fma_f32 v5, v44, v52, v53
	v_fma_f32 v8, v41, v52, v53
	v_fma_f32 v10, v12, v14, v10
	v_fma_f32 v12, v46, v52, v53
	s_waitcnt lgkmcnt(0)
	v_fma_f32 v5, v5, v16, v20
	v_fma_f32 v8, v8, v13, v9
	v_fma_f32 v9, v45, v52, v53
	v_fma_f32 v16, v12, v18, v22
	v_fma_f32 v12, v43, v52, v53
	v_fma_f32 v9, v9, v17, v21
	v_fmac_f32_e32 v11, v12, v15
	v_fma_f32 v12, v47, v52, v53
	v_fmac_f32_e32 v23, v12, v19
	v_cvt_pk_bf16_f32 v12, v4, v8
	v_cvt_pk_bf16_f32 v13, v10, v11
	v_cvt_pk_bf16_f32 v14, v5, v9
	v_cvt_pk_fp8_f32 v4, v4, v8
	v_cvt_pk_fp8_f32 v5, v5, v9
	v_cvt_pk_bf16_f32 v15, v16, v23
	global_store_dwordx4 v[26:27], v[12:15], off offset:2048
	v_cvt_pk_fp8_f32 v4, v10, v11 op_sel:[0,0,1]
	v_cvt_pk_fp8_f32 v5, v16, v23 op_sel:[0,0,1]
	ds_read_b128 v[8:11], v112 offset:18432
	ds_read_b128 v[12:15], v112 offset:10240
	ds_read_b128 v[16:19], v112 offset:10256
	ds_read_b128 v[20:23], v112 offset:18448
	global_store_dwordx2 v[28:29], v[4:5], off offset:1024
	v_fma_f32 v4, v48, v52, v53
	s_waitcnt lgkmcnt(2)
	v_fma_f32 v24, v4, v12, v8
	v_fma_f32 v4, v7, v52, v53
	s_waitcnt lgkmcnt(0)
	v_fma_f32 v25, v4, v16, v20
	v_fma_f32 v4, v49, v52, v53
	v_fma_f32 v7, v4, v13, v9
	v_fma_f32 v4, v6, v52, v53
	v_fma_f32 v8, v4, v17, v21
	v_fma_f32 v4, v50, v52, v53
	v_fma_f32 v9, v4, v14, v10
	v_fma_f32 v4, v51, v52, v53
	v_fmac_f32_e32 v11, v4, v15
	v_cvt_pk_bf16_f32 v4, v24, v7
	v_cvt_pk_bf16_f32 v5, v9, v11
	v_cvt_pk_bf16_f32 v6, v25, v8
	v_cvt_pk_fp8_f32 v24, v24, v7
	v_cvt_pk_fp8_f32 v25, v25, v8
	v_fmac_f32_e32 v53, v2, v52
	v_fma_f32 v3, v3, v18, v22
	v_fmac_f32_e32 v23, v53, v19
	v_cvt_pk_fp8_f32 v24, v9, v11 op_sel:[0,0,1]
	v_cvt_pk_fp8_f32 v25, v3, v23 op_sel:[0,0,1]
	v_cvt_pk_bf16_f32 v7, v3, v23
	global_store_dwordx4 v[26:27], v[4:7], off offset:3072
	global_store_dwordx2 v[28:29], v[24:25], off offset:1536
	s_mov_b32 s0, 4
	s_andn2_b64 vcc, exec, s[26:27]
	s_mov_b64 s[26:27], 0
	s_cbranch_vccz .LBB0_1026
	v_ashrrev_i32_e32 v83, 31, v82
	s_waitcnt vmcnt(0)
	v_lshlrev_b64 v[2:3], 12, v[82:83]
	v_mov_b32_e32 v30, 0
	v_lshl_add_u64 v[84:85], v[80:81], 0, v[2:3]
	s_mov_b64 s[42:43], 0
	v_mov_b32_e32 v31, v30
	v_mov_b32_e32 v32, v30
	v_mov_b32_e32 v33, v30
	v_mov_b32_e32 v6, v30
	v_mov_b32_e32 v7, v30
	v_mov_b32_e32 v8, v30
	v_mov_b32_e32 v9, v30
	v_mov_b32_e32 v14, v30
	v_mov_b32_e32 v15, v30
	v_mov_b32_e32 v16, v30
	v_mov_b32_e32 v17, v30
	v_mov_b32_e32 v26, v30
	v_mov_b32_e32 v27, v30
	v_mov_b32_e32 v28, v30
	v_mov_b32_e32 v29, v30
	v_mov_b32_e32 v2, v30
	v_mov_b32_e32 v3, v30
	v_mov_b32_e32 v4, v30
	v_mov_b32_e32 v5, v30
	v_mov_b32_e32 v10, v30
	v_mov_b32_e32 v11, v30
	v_mov_b32_e32 v12, v30
	v_mov_b32_e32 v13, v30
	v_mov_b32_e32 v18, v30
	v_mov_b32_e32 v19, v30
	v_mov_b32_e32 v20, v30
	v_mov_b32_e32 v21, v30
	v_mov_b32_e32 v34, v30
	v_mov_b32_e32 v35, v30
	v_mov_b32_e32 v36, v30
	v_mov_b32_e32 v37, v30
	v_mov_b32_e32 v38, v30
	v_mov_b32_e32 v39, v30
	v_mov_b32_e32 v40, v30
	v_mov_b32_e32 v41, v30
	v_mov_b32_e32 v42, v30
	v_mov_b32_e32 v43, v30
	v_mov_b32_e32 v44, v30
	v_mov_b32_e32 v45, v30
	v_mov_b32_e32 v46, v30
	v_mov_b32_e32 v47, v30
	v_mov_b32_e32 v48, v30
	v_mov_b32_e32 v49, v30
	v_mov_b32_e32 v50, v30
	v_mov_b32_e32 v51, v30
	v_mov_b32_e32 v52, v30
	v_mov_b32_e32 v53, v30
	v_mov_b32_e32 v54, v30
	v_mov_b32_e32 v55, v30
	v_mov_b32_e32 v56, v30
	v_mov_b32_e32 v57, v30
	v_mov_b32_e32 v58, v30
	v_mov_b32_e32 v59, v30
	v_mov_b32_e32 v60, v30
	v_mov_b32_e32 v61, v30
	v_mov_b32_e32 v62, v30
	v_mov_b32_e32 v63, v30
	v_mov_b32_e32 v64, v30
	v_mov_b32_e32 v65, v30
	v_mov_b32_e32 v22, v30
	v_mov_b32_e32 v23, v30
	v_mov_b32_e32 v24, v30
	v_mov_b32_e32 v25, v30
	s_barrier

.LBB0_1734:
	v_ashrrev_i32_e32 v73, 31, v72
	v_ashrrev_i32_e32 v67, 31, v66
	v_lshl_add_u64 v[80:81], v[72:73], 2, s[8:9]
	v_lshlrev_b64 v[82:83], 12, v[66:67]
	global_load_dword v100, v[80:81], off sc1
	global_load_dword v102, v[80:81], off offset:4 sc1
	global_load_dword v104, v[80:81], off offset:8 sc1
	global_load_dword v106, v[80:81], off offset:12 sc1
	global_load_dword v108, v[80:81], off offset:16 sc1
	global_load_dword v110, v[80:81], off offset:20 sc1
	global_load_dword v112, v[80:81], off offset:24 sc1
	global_load_dword v114, v[80:81], off offset:28 sc1
	v_lshlrev_b64 v[84:85], 13, v[66:67]
	v_lshl_add_u64 v[80:81], v[70:71], 0, v[82:83]
	v_lshl_add_u64 v[124:125], s[10:11], 0, v[84:85]
	global_load_dwordx4 v[84:87], v[80:81], off offset:3072
	global_load_dwordx4 v[88:91], v[80:81], off
	global_load_dwordx4 v[92:95], v[80:81], off offset:1024
	global_load_dwordx4 v[96:99], v[80:81], off offset:2048
	v_add_u32_e32 v78, v116, v66
	v_ashrrev_i32_e32 v79, 31, v78
	v_lshlrev_b64 v[78:79], 11, v[78:79]
	v_mov_b32_e32 v75, v65
	v_mov_b32_e32 v77, v65
	v_lshl_add_u64 v[126:127], v[68:69], 0, v[78:79]
	v_lshl_add_u64 v[82:83], v[124:125], 0, v[64:65]
	v_lshl_add_u64 v[80:81], v[124:125], 0, v[74:75]
	v_lshl_add_u64 v[78:79], v[124:125], 0, v[76:77]
	global_load_dwordx2 v[124:125], v[126:127], off
	global_load_dwordx2 v[128:129], v[126:127], off offset:512
	global_load_dwordx2 v[130:131], v[126:127], off offset:1024
	global_load_dwordx2 v[132:133], v[126:127], off offset:1536
	v_add_u32_e32 v66, s5, v66
	v_cmp_lt_i32_e32 vcc, s7, v66
	s_or_b64 s[0:1], vcc, s[0:1]
	v_add_u32_e32 v72, s3, v72
	s_waitcnt vmcnt(15)
	v_ashrrev_i32_e32 v101, 31, v100
	s_waitcnt vmcnt(14)
	v_ashrrev_i32_e32 v103, 31, v102
	s_waitcnt vmcnt(13)
	v_ashrrev_i32_e32 v105, 31, v104
	s_waitcnt vmcnt(12)
	v_ashrrev_i32_e32 v107, 31, v106
	s_waitcnt vmcnt(11)
	v_ashrrev_i32_e32 v109, 31, v108
	s_waitcnt vmcnt(10)
	v_ashrrev_i32_e32 v111, 31, v110
	s_waitcnt vmcnt(9)
	v_ashrrev_i32_e32 v113, 31, v112
	s_waitcnt vmcnt(8)
	v_ashrrev_i32_e32 v115, 31, v114
	v_lshlrev_b64 v[100:101], 11, v[100:101]
	v_lshlrev_b64 v[102:103], 11, v[102:103]
	v_lshlrev_b64 v[104:105], 11, v[104:105]
	v_lshlrev_b64 v[106:107], 11, v[106:107]
	v_lshlrev_b64 v[108:109], 11, v[108:109]
	v_lshlrev_b64 v[110:111], 11, v[110:111]
	v_lshlrev_b64 v[112:113], 11, v[112:113]
	v_lshlrev_b64 v[114:115], 11, v[114:115]
	s_waitcnt vmcnt(7)
	v_and_b32_e32 v127, 0xffff0000, v86
	v_lshlrev_b32_e32 v126, 16, v86
	v_and_b32_e32 v135, 0xffff0000, v87
	v_lshlrev_b32_e32 v134, 16, v87
	s_waitcnt vmcnt(6)
	v_lshlrev_b32_e32 v136, 16, v90
	v_and_b32_e32 v137, 0xffff0000, v90
	v_lshlrev_b32_e32 v138, 16, v88
	v_and_b32_e32 v139, 0xffff0000, v88
	v_lshlrev_b32_e32 v140, 16, v89
	v_and_b32_e32 v141, 0xffff0000, v89
	s_waitcnt vmcnt(5)
	v_lshlrev_b32_e32 v142, 16, v94
	v_and_b32_e32 v143, 0xffff0000, v94
	v_lshlrev_b32_e32 v144, 16, v95
	v_and_b32_e32 v145, 0xffff0000, v95
	v_lshlrev_b32_e32 v146, 16, v92
	v_and_b32_e32 v147, 0xffff0000, v92
	v_lshlrev_b32_e32 v148, 16, v93
	v_and_b32_e32 v149, 0xffff0000, v93
	s_waitcnt vmcnt(4)
	v_lshlrev_b32_e32 v150, 16, v98
	v_and_b32_e32 v151, 0xffff0000, v98
	v_lshlrev_b32_e32 v152, 16, v99
	v_and_b32_e32 v153, 0xffff0000, v99
	v_lshlrev_b32_e32 v154, 16, v96
	v_and_b32_e32 v155, 0xffff0000, v96
	v_lshlrev_b32_e32 v156, 16, v97
	v_and_b32_e32 v157, 0xffff0000, v97
	v_lshlrev_b32_e32 v158, 16, v84
	v_and_b32_e32 v159, 0xffff0000, v84
	v_lshlrev_b32_e32 v160, 16, v85
	v_and_b32_e32 v161, 0xffff0000, v85
	v_lshl_add_u64 v[186:187], v[68:69], 0, v[100:101]
	v_lshl_add_u64 v[188:189], v[68:69], 0, v[102:103]
	v_lshl_add_u64 v[190:191], v[68:69], 0, v[104:105]
	v_lshl_add_u64 v[192:193], v[68:69], 0, v[106:107]
	v_lshl_add_u64 v[194:195], v[68:69], 0, v[108:109]
	v_lshl_add_u64 v[196:197], v[68:69], 0, v[110:111]
	v_lshl_add_u64 v[198:199], v[68:69], 0, v[112:113]
	v_lshl_add_u64 v[200:201], v[68:69], 0, v[114:115]
	v_pk_mul_f32 v[84:85], v[126:127], s[4:5] op_sel_hi:[1,0]
	v_pk_mul_f32 v[86:87], v[134:135], s[4:5] op_sel_hi:[1,0]
	v_pk_mul_f32 v[88:89], v[136:137], s[4:5] op_sel_hi:[1,0]
	v_pk_mul_f32 v[92:93], v[138:139], s[4:5] op_sel_hi:[1,0]
	v_pk_mul_f32 v[94:95], v[140:141], s[4:5] op_sel_hi:[1,0]
	v_pk_mul_f32 v[96:97], v[142:143], s[4:5] op_sel_hi:[1,0]
	v_pk_mul_f32 v[98:99], v[144:145], s[4:5] op_sel_hi:[1,0]
	v_pk_mul_f32 v[100:101], v[146:147], s[4:5] op_sel_hi:[1,0]
	v_pk_mul_f32 v[102:103], v[148:149], s[4:5] op_sel_hi:[1,0]
	v_pk_mul_f32 v[104:105], v[150:151], s[4:5] op_sel_hi:[1,0]
	v_pk_mul_f32 v[106:107], v[152:153], s[4:5] op_sel_hi:[1,0]
	v_pk_mul_f32 v[108:109], v[154:155], s[4:5] op_sel_hi:[1,0]
	v_pk_mul_f32 v[110:111], v[156:157], s[4:5] op_sel_hi:[1,0]
	v_pk_mul_f32 v[112:113], v[158:159], s[4:5] op_sel_hi:[1,0]
	v_pk_mul_f32 v[114:115], v[160:161], s[4:5] op_sel_hi:[1,0]
	global_load_dwordx2 v[126:127], v[186:187], off
	global_load_dwordx2 v[134:135], v[186:187], off offset:512
	global_load_dwordx2 v[136:137], v[186:187], off offset:1024
	global_load_dwordx2 v[138:139], v[186:187], off offset:1536
	global_load_dwordx2 v[140:141], v[188:189], off
	global_load_dwordx2 v[142:143], v[188:189], off offset:512
	global_load_dwordx2 v[144:145], v[188:189], off offset:1024
	global_load_dwordx2 v[146:147], v[188:189], off offset:1536
	global_load_dwordx2 v[148:149], v[190:191], off
	global_load_dwordx2 v[150:151], v[190:191], off offset:512
	global_load_dwordx2 v[152:153], v[190:191], off offset:1024
	global_load_dwordx2 v[154:155], v[190:191], off offset:1536
	global_load_dwordx2 v[156:157], v[192:193], off
	global_load_dwordx2 v[158:159], v[192:193], off offset:512
	global_load_dwordx2 v[160:161], v[192:193], off offset:1024
	global_load_dwordx2 v[186:187], v[192:193], off offset:1536
	global_load_dwordx2 v[188:189], v[194:195], off
	global_load_dwordx2 v[190:191], v[194:195], off offset:512
	s_nop 0
	global_load_dwordx2 v[192:193], v[194:195], off offset:1024
	s_nop 0
	global_load_dwordx2 v[194:195], v[194:195], off offset:1536
	s_nop 0
	global_load_dwordx2 v[202:203], v[196:197], off
	global_load_dwordx2 v[204:205], v[196:197], off offset:512
	global_load_dwordx2 v[206:207], v[196:197], off offset:1024
	s_nop 0
	global_load_dwordx2 v[196:197], v[196:197], off offset:1536
	s_nop 0
	global_load_dwordx2 v[208:209], v[198:199], off
	global_load_dwordx2 v[210:211], v[198:199], off offset:512
	global_load_dwordx2 v[212:213], v[198:199], off offset:1024
	s_nop 0
	global_load_dwordx2 v[198:199], v[198:199], off offset:1536
	s_nop 0
	global_load_dwordx2 v[214:215], v[200:201], off
	global_load_dwordx2 v[216:217], v[200:201], off offset:512
	global_load_dwordx2 v[218:219], v[200:201], off offset:1024
	s_nop 0
	global_load_dwordx2 v[200:201], v[200:201], off offset:1536
	s_waitcnt vmcnt(35)
	v_cvt_pk_f32_fp8_e32 v[162:163], v124
	v_cvt_pk_f32_fp8_sdwa v[164:165], v124 src0_sel:WORD_1
	v_cvt_pk_f32_fp8_e32 v[166:167], v125
	v_cvt_pk_f32_fp8_sdwa v[124:125], v125 src0_sel:WORD_1
	s_waitcnt vmcnt(34)
	v_cvt_pk_f32_fp8_e32 v[168:169], v128
	v_cvt_pk_f32_fp8_sdwa v[170:171], v128 src0_sel:WORD_1
	v_cvt_pk_f32_fp8_e32 v[172:173], v129
	v_cvt_pk_f32_fp8_sdwa v[128:129], v129 src0_sel:WORD_1
	s_waitcnt vmcnt(33)
	v_cvt_pk_f32_fp8_e32 v[174:175], v130
	v_cvt_pk_f32_fp8_sdwa v[176:177], v130 src0_sel:WORD_1
	v_cvt_pk_f32_fp8_e32 v[178:179], v131
	v_cvt_pk_f32_fp8_sdwa v[130:131], v131 src0_sel:WORD_1
	s_waitcnt vmcnt(32)
	v_cvt_pk_f32_fp8_e32 v[180:181], v132
	v_cvt_pk_f32_fp8_sdwa v[182:183], v132 src0_sel:WORD_1
	v_cvt_pk_f32_fp8_e32 v[184:185], v133
	v_cvt_pk_f32_fp8_sdwa v[132:133], v133 src0_sel:WORD_1
	v_pk_add_f32 v[162:163], v[162:163], 0 op_sel_hi:[1,0]
	v_pk_add_f32 v[164:165], v[164:165], 0 op_sel_hi:[1,0]
	v_pk_add_f32 v[166:167], v[166:167], 0 op_sel_hi:[1,0]
	v_pk_add_f32 v[124:125], v[124:125], 0 op_sel_hi:[1,0]
	v_pk_add_f32 v[168:169], v[168:169], 0 op_sel_hi:[1,0]
	v_pk_add_f32 v[170:171], v[170:171], 0 op_sel_hi:[1,0]
	v_pk_add_f32 v[172:173], v[172:173], 0 op_sel_hi:[1,0]
	v_pk_add_f32 v[128:129], v[128:129], 0 op_sel_hi:[1,0]
	v_pk_add_f32 v[174:175], v[174:175], 0 op_sel_hi:[1,0]
	v_pk_add_f32 v[176:177], v[176:177], 0 op_sel_hi:[1,0]
	v_pk_add_f32 v[130:131], v[130:131], 0 op_sel_hi:[1,0]
	v_pk_add_f32 v[180:181], v[180:181], 0 op_sel_hi:[1,0]
	v_pk_add_f32 v[182:183], v[182:183], 0 op_sel_hi:[1,0]
	v_pk_add_f32 v[184:185], v[184:185], 0 op_sel_hi:[1,0]
	v_pk_add_f32 v[132:133], v[132:133], 0 op_sel_hi:[1,0]
	v_pk_add_f32 v[178:179], v[178:179], 0 op_sel_hi:[1,0]
	v_lshlrev_b32_e32 v90, 16, v91
	v_and_b32_e32 v91, 0xffff0000, v91
	v_pk_mul_f32 v[90:91], v[90:91], s[4:5] op_sel_hi:[1,0]
	s_waitcnt vmcnt(31)
	v_cvt_pk_f32_fp8_e32 v[220:221], v126
	v_cvt_pk_f32_fp8_sdwa v[222:223], v126 src0_sel:WORD_1
	v_cvt_pk_f32_fp8_e32 v[224:225], v127
	v_cvt_pk_f32_fp8_sdwa v[126:127], v127 src0_sel:WORD_1
	s_waitcnt vmcnt(30)
	v_cvt_pk_f32_fp8_e32 v[226:227], v134
	v_cvt_pk_f32_fp8_sdwa v[228:229], v134 src0_sel:WORD_1
	v_cvt_pk_f32_fp8_e32 v[230:231], v135
	v_cvt_pk_f32_fp8_sdwa v[134:135], v135 src0_sel:WORD_1
	s_waitcnt vmcnt(29)
	v_cvt_pk_f32_fp8_e32 v[232:233], v136
	v_cvt_pk_f32_fp8_sdwa v[234:235], v136 src0_sel:WORD_1
	v_cvt_pk_f32_fp8_e32 v[236:237], v137
	v_cvt_pk_f32_fp8_sdwa v[136:137], v137 src0_sel:WORD_1
	s_waitcnt vmcnt(28)
	v_cvt_pk_f32_fp8_e32 v[238:239], v138
	v_cvt_pk_f32_fp8_sdwa v[240:241], v138 src0_sel:WORD_1
	v_cvt_pk_f32_fp8_e32 v[242:243], v139
	v_cvt_pk_f32_fp8_sdwa v[138:139], v139 src0_sel:WORD_1
	s_waitcnt vmcnt(27)
	v_cvt_pk_f32_fp8_e32 v[244:245], v140
	v_cvt_pk_f32_fp8_sdwa v[246:247], v140 src0_sel:WORD_1
	s_waitcnt vmcnt(26)
	v_cvt_pk_f32_fp8_e32 v[250:251], v142
	v_pk_add_f32 v[162:163], v[162:163], v[220:221]
	v_cvt_pk_f32_fp8_sdwa v[220:221], v142 src0_sel:WORD_1
	v_pk_add_f32 v[164:165], v[164:165], v[222:223]
	v_cvt_pk_f32_fp8_e32 v[222:223], v143
	v_cvt_pk_f32_fp8_sdwa v[142:143], v143 src0_sel:WORD_1
	v_pk_add_f32 v[166:167], v[166:167], v[224:225]
	s_waitcnt vmcnt(25)
	v_cvt_pk_f32_fp8_e32 v[224:225], v144
	v_pk_add_f32 v[124:125], v[124:125], v[126:127]
	v_cvt_pk_f32_fp8_sdwa v[126:127], v144 src0_sel:WORD_1
	v_cvt_pk_f32_fp8_e32 v[248:249], v141
	v_cvt_pk_f32_fp8_sdwa v[140:141], v141 src0_sel:WORD_1
	v_pk_add_f32 v[168:169], v[168:169], v[226:227]
	v_cvt_pk_f32_fp8_e32 v[226:227], v145
	v_cvt_pk_f32_fp8_sdwa v[144:145], v145 src0_sel:WORD_1
	v_pk_add_f32 v[170:171], v[170:171], v[228:229]
	s_waitcnt vmcnt(24)
	v_cvt_pk_f32_fp8_e32 v[228:229], v146
	v_pk_add_f32 v[172:173], v[172:173], v[230:231]
	v_cvt_pk_f32_fp8_sdwa v[230:231], v146 src0_sel:WORD_1
	v_pk_add_f32 v[128:129], v[128:129], v[134:135]
	v_cvt_pk_f32_fp8_e32 v[134:135], v147
	v_cvt_pk_f32_fp8_sdwa v[146:147], v147 src0_sel:WORD_1
	v_pk_add_f32 v[174:175], v[174:175], v[232:233]
	s_waitcnt vmcnt(23)
	v_cvt_pk_f32_fp8_e32 v[232:233], v148
	v_pk_add_f32 v[176:177], v[176:177], v[234:235]
	v_pk_add_f32 v[130:131], v[130:131], v[136:137]
	s_waitcnt vmcnt(22)
	v_cvt_pk_f32_fp8_e32 v[136:137], v150
	v_pk_add_f32 v[180:181], v[180:181], v[238:239]
	v_cvt_pk_f32_fp8_sdwa v[238:239], v150 src0_sel:WORD_1
	v_pk_add_f32 v[182:183], v[182:183], v[240:241]
	v_cvt_pk_f32_fp8_e32 v[240:241], v151
	v_cvt_pk_f32_fp8_sdwa v[150:151], v151 src0_sel:WORD_1
	v_pk_add_f32 v[184:185], v[184:185], v[242:243]
	s_waitcnt vmcnt(21)
	v_cvt_pk_f32_fp8_e32 v[242:243], v152
	v_pk_add_f32 v[132:133], v[132:133], v[138:139]
	v_cvt_pk_f32_fp8_sdwa v[138:139], v152 src0_sel:WORD_1
	v_pk_add_f32 v[162:163], v[162:163], v[244:245]
	v_cvt_pk_f32_fp8_e32 v[244:245], v153
	v_cvt_pk_f32_fp8_sdwa v[152:153], v153 src0_sel:WORD_1
	v_cvt_pk_f32_fp8_sdwa v[234:235], v148 src0_sel:WORD_1
	v_pk_add_f32 v[164:165], v[164:165], v[246:247]
	s_waitcnt vmcnt(20)
	v_cvt_pk_f32_fp8_e32 v[246:247], v154
	v_pk_add_f32 v[128:129], v[128:129], v[142:143]
	s_waitcnt vmcnt(18)
	v_cvt_pk_f32_fp8_e32 v[142:143], v158
	v_pk_add_f32 v[174:175], v[174:175], v[224:225]
	v_cvt_pk_f32_fp8_sdwa v[224:225], v158 src0_sel:WORD_1
	v_pk_add_f32 v[126:127], v[176:177], v[126:127]
	v_cvt_pk_f32_fp8_e32 v[176:177], v159
	v_cvt_pk_f32_fp8_sdwa v[158:159], v159 src0_sel:WORD_1
	v_pk_add_f32 v[124:125], v[124:125], v[140:141]
	v_cvt_pk_f32_fp8_e32 v[140:141], v155
	v_pk_add_f32 v[168:169], v[168:169], v[250:251]
	v_cvt_pk_f32_fp8_e32 v[250:251], v156
	v_pk_add_f32 v[166:167], v[166:167], v[248:249]
	v_cvt_pk_f32_fp8_sdwa v[248:249], v154 src0_sel:WORD_1
	v_pk_add_f32 v[130:131], v[130:131], v[144:145]
	v_pk_add_f32 v[132:133], v[132:133], v[146:147]
	s_waitcnt vmcnt(16)
	v_cvt_pk_f32_fp8_e32 v[146:147], v187
	v_pk_add_f32 v[162:163], v[162:163], v[232:233]
	s_waitcnt vmcnt(15)
	v_cvt_pk_f32_fp8_e32 v[232:233], v188
	v_pk_add_f32 v[178:179], v[178:179], v[236:237]
	v_cvt_pk_f32_fp8_e32 v[236:237], v149
	v_pk_add_f32 v[170:171], v[170:171], v[220:221]
	v_cvt_pk_f32_fp8_sdwa v[220:221], v156 src0_sel:WORD_1
	v_pk_add_f32 v[180:181], v[180:181], v[228:229]
	v_pk_add_f32 v[128:129], v[128:129], v[150:151]
	v_pk_add_f32 v[130:131], v[130:131], v[152:153]
	s_waitcnt vmcnt(12)
	v_cvt_pk_f32_fp8_e32 v[152:153], v195
	v_pk_add_f32 v[134:135], v[184:185], v[134:135]
	v_pk_add_f32 v[164:165], v[164:165], v[234:235]
	v_cvt_pk_f32_fp8_sdwa v[234:235], v188 src0_sel:WORD_1
	v_pk_add_f32 v[136:137], v[168:169], v[136:137]
	v_pk_add_f32 v[180:181], v[180:181], v[246:247]
	s_waitcnt vmcnt(11)
	v_cvt_pk_f32_fp8_e32 v[246:247], v202
	v_pk_add_f32 v[128:129], v[128:129], v[158:159]
	s_waitcnt vmcnt(8)
	v_cvt_pk_f32_fp8_e32 v[158:159], v197
	v_cvt_pk_f32_fp8_e32 v[228:229], v161
	v_pk_add_f32 v[182:183], v[182:183], v[230:231]
	v_pk_add_f32 v[134:135], v[134:135], v[140:141]
	v_pk_add_f32 v[162:163], v[162:163], v[250:251]
	v_pk_add_f32 v[136:137], v[136:137], v[142:143]
	s_waitcnt vmcnt(7)
	v_cvt_pk_f32_fp8_e32 v[142:143], v208
	v_cvt_pk_f32_fp8_sdwa v[148:149], v149 src0_sel:WORD_1
	v_pk_add_f32 v[172:173], v[172:173], v[222:223]
	v_cvt_pk_f32_fp8_e32 v[222:223], v157
	v_pk_add_f32 v[170:171], v[170:171], v[238:239]
	v_cvt_pk_f32_fp8_e32 v[238:239], v191
	v_pk_add_f32 v[182:183], v[182:183], v[248:249]
	v_cvt_pk_f32_fp8_sdwa v[248:249], v202 src0_sel:WORD_1
	v_pk_add_f32 v[134:135], v[134:135], v[146:147]
	v_pk_add_f32 v[162:163], v[162:163], v[232:233]
	s_waitcnt vmcnt(3)
	v_cvt_pk_f32_fp8_e32 v[232:233], v214
	v_pk_add_f32 v[178:179], v[178:179], v[226:227]
	v_pk_add_f32 v[166:167], v[166:167], v[236:237]
	v_cvt_pk_f32_fp8_e32 v[236:237], v189
	v_pk_add_f32 v[164:165], v[164:165], v[220:221]
	v_pk_add_f32 v[170:171], v[170:171], v[224:225]
	v_cvt_pk_f32_fp8_sdwa v[224:225], v208 src0_sel:WORD_1
	v_pk_add_f32 v[134:135], v[134:135], v[152:153]
	v_cvt_pk_f32_fp8_sdwa v[154:155], v155 src0_sel:WORD_1
	v_cvt_pk_f32_fp8_sdwa v[156:157], v157 src0_sel:WORD_1
	v_pk_add_f32 v[172:173], v[172:173], v[240:241]
	v_pk_add_f32 v[178:179], v[178:179], v[244:245]
	v_cvt_pk_f32_fp8_e32 v[140:141], v203
	v_pk_add_f32 v[164:165], v[164:165], v[234:235]
	v_cvt_pk_f32_fp8_sdwa v[234:235], v214 src0_sel:WORD_1
	v_pk_add_f32 v[134:135], v[134:135], v[158:159]
	v_pk_add_f32 v[158:159], v[162:163], v[246:247]
	v_cvt_pk_f32_fp8_e32 v[226:227], v160
	v_cvt_pk_f32_fp8_sdwa v[144:145], v160 src0_sel:WORD_1
	v_cvt_pk_f32_fp8_sdwa v[160:161], v161 src0_sel:WORD_1
	v_cvt_pk_f32_fp8_sdwa v[188:189], v189 src0_sel:WORD_1
	v_pk_add_f32 v[172:173], v[172:173], v[176:177]
	v_pk_add_f32 v[178:179], v[178:179], v[228:229]
	v_cvt_pk_f32_fp8_e32 v[228:229], v209
	v_pk_add_f32 v[142:143], v[158:159], v[142:143]
	v_pk_add_f32 v[124:125], v[124:125], v[148:149]
	v_cvt_pk_f32_fp8_e32 v[148:149], v190
	v_cvt_pk_f32_fp8_sdwa v[168:169], v190 src0_sel:WORD_1
	v_cvt_pk_f32_fp8_sdwa v[190:191], v191 src0_sel:WORD_1
	v_cvt_pk_f32_fp8_sdwa v[202:203], v203 src0_sel:WORD_1
	v_pk_add_f32 v[166:167], v[166:167], v[222:223]
	v_pk_add_f32 v[172:173], v[172:173], v[238:239]
	v_cvt_pk_f32_fp8_e32 v[238:239], v215
	v_pk_add_f32 v[162:163], v[164:165], v[248:249]
	v_pk_add_f32 v[142:143], v[142:143], v[232:233]
	v_cvt_pk_f32_fp8_sdwa v[208:209], v209 src0_sel:WORD_1
	v_pk_add_f32 v[166:167], v[166:167], v[236:237]
	v_pk_add_f32 v[158:159], v[162:163], v[224:225]
	v_pk_fma_f32 v[92:93], v[142:143], s[2:3], v[92:93] op_sel_hi:[1,0,1]
	v_cvt_pk_f32_fp8_e32 v[230:231], v186
	v_cvt_pk_f32_fp8_sdwa v[184:185], v186 src0_sel:WORD_1
	v_cvt_pk_f32_fp8_sdwa v[186:187], v187 src0_sel:WORD_1
	v_pk_add_f32 v[132:133], v[132:133], v[154:155]
	v_cvt_pk_f32_fp8_e32 v[154:155], v204
	v_pk_add_f32 v[124:125], v[124:125], v[156:157]
	v_cvt_pk_f32_fp8_sdwa v[214:215], v215 src0_sel:WORD_1
	v_pk_add_f32 v[140:141], v[166:167], v[140:141]
	v_pk_add_f32 v[158:159], v[158:159], v[234:235]
	v_add_f32_e32 v67, 0, v92
	v_pk_add_f32 v[130:131], v[130:131], v[160:161]
	v_cvt_pk_f32_fp8_e32 v[160:161], v210
	v_pk_add_f32 v[124:125], v[124:125], v[188:189]
	v_pk_add_f32 v[140:141], v[140:141], v[228:229]
	v_pk_fma_f32 v[94:95], v[158:159], s[2:3], v[94:95] op_sel_hi:[1,0,1]
	v_add_f32_e32 v67, v93, v67
	v_pk_add_f32 v[174:175], v[174:175], v[242:243]
	v_cvt_pk_f32_fp8_sdwa v[146:147], v204 src0_sel:WORD_1
	v_pk_add_f32 v[128:129], v[128:129], v[190:191]
	s_waitcnt vmcnt(2)
	v_cvt_pk_f32_fp8_e32 v[190:191], v216
	v_pk_add_f32 v[124:125], v[124:125], v[202:203]
	v_pk_add_f32 v[140:141], v[140:141], v[238:239]
	v_add_f32_e32 v67, v94, v67
	v_pk_add_f32 v[174:175], v[174:175], v[226:227]
	v_cvt_pk_f32_fp8_sdwa v[226:227], v210 src0_sel:WORD_1
	v_pk_add_f32 v[136:137], v[136:137], v[148:149]
	v_pk_add_f32 v[124:125], v[124:125], v[208:209]
	v_pk_fma_f32 v[88:89], v[140:141], s[2:3], v[88:89] op_sel_hi:[1,0,1]
	v_add_f32_e32 v67, v95, v67
	v_pk_add_f32 v[126:127], v[126:127], v[138:139]
	v_pk_add_f32 v[132:133], v[132:133], v[186:187]
	v_cvt_pk_f32_fp8_e32 v[186:187], v205
	v_cvt_pk_f32_fp8_sdwa v[148:149], v216 src0_sel:WORD_1
	v_pk_add_f32 v[136:137], v[136:137], v[154:155]
	v_pk_add_f32 v[124:125], v[124:125], v[214:215]
	v_add_f32_e32 v67, v88, v67
	v_pk_add_f32 v[126:127], v[126:127], v[144:145]
	v_cvt_pk_f32_fp8_e32 v[144:145], v211
	v_pk_add_f32 v[168:169], v[170:171], v[168:169]
	v_pk_add_f32 v[136:137], v[136:137], v[160:161]
	v_pk_fma_f32 v[90:91], v[124:125], s[2:3], v[90:91] op_sel_hi:[1,0,1]
	v_add_f32_e32 v67, v89, v67
	v_cvt_pk_f32_fp8_e32 v[240:241], v192
	v_cvt_pk_f32_fp8_e32 v[242:243], v193
	v_cvt_pk_f32_fp8_sdwa v[204:205], v205 src0_sel:WORD_1
	v_cvt_pk_f32_fp8_e32 v[170:171], v217
	v_pk_add_f32 v[146:147], v[168:169], v[146:147]
	v_pk_add_f32 v[136:137], v[136:137], v[190:191]
	v_add_f32_e32 v67, v90, v67
	v_cvt_pk_f32_fp8_sdwa v[210:211], v211 src0_sel:WORD_1
	v_pk_add_f32 v[146:147], v[146:147], v[226:227]
	v_pk_fma_f32 v[100:101], v[136:137], s[2:3], v[100:101] op_sel_hi:[1,0,1]
	v_add_f32_e32 v67, v91, v67
	v_cvt_pk_f32_fp8_sdwa v[150:151], v192 src0_sel:WORD_1
	v_cvt_pk_f32_fp8_sdwa v[192:193], v193 src0_sel:WORD_1
	v_cvt_pk_f32_fp8_e32 v[222:223], v206
	v_cvt_pk_f32_fp8_e32 v[250:251], v207
	v_cvt_pk_f32_fp8_sdwa v[216:217], v217 src0_sel:WORD_1
	v_pk_add_f32 v[164:165], v[172:173], v[186:187]
	v_pk_add_f32 v[146:147], v[146:147], v[148:149]
	v_add_f32_e32 v67, v100, v67
	v_pk_add_f32 v[180:181], v[180:181], v[230:231]
	v_cvt_pk_f32_fp8_e32 v[230:231], v212
	v_cvt_pk_f32_fp8_e32 v[152:153], v213
	v_pk_add_f32 v[144:145], v[164:165], v[144:145]
	v_pk_fma_f32 v[102:103], v[146:147], s[2:3], v[102:103] op_sel_hi:[1,0,1]
	v_add_f32_e32 v67, v101, v67
	v_cvt_pk_f32_fp8_sdwa v[156:157], v206 src0_sel:WORD_1
	v_pk_add_f32 v[178:179], v[178:179], v[242:243]
	s_waitcnt vmcnt(1)
	v_cvt_pk_f32_fp8_e32 v[242:243], v218
	v_pk_add_f32 v[174:175], v[174:175], v[240:241]
	v_cvt_pk_f32_fp8_e32 v[240:241], v219
	v_pk_add_f32 v[128:129], v[128:129], v[204:205]
	v_pk_add_f32 v[144:145], v[144:145], v[170:171]
	v_add_f32_e32 v67, v102, v67
	v_pk_add_f32 v[182:183], v[182:183], v[184:185]
	v_cvt_pk_f32_fp8_sdwa v[184:185], v212 src0_sel:WORD_1
	v_pk_add_f32 v[128:129], v[128:129], v[210:211]
	v_pk_fma_f32 v[96:97], v[144:145], s[2:3], v[96:97] op_sel_hi:[1,0,1]
	v_add_f32_e32 v67, v103, v67
	v_pk_add_f32 v[130:131], v[130:131], v[192:193]
	v_cvt_pk_f32_fp8_sdwa v[192:193], v218 src0_sel:WORD_1
	v_pk_add_f32 v[154:155], v[178:179], v[250:251]
	v_pk_add_f32 v[166:167], v[174:175], v[222:223]
	v_pk_add_f32 v[128:129], v[128:129], v[216:217]
	v_add_f32_e32 v67, v96, v67
	v_cvt_pk_f32_fp8_e32 v[138:139], v194
	v_cvt_pk_f32_fp8_sdwa v[244:245], v194 src0_sel:WORD_1
	v_cvt_pk_f32_fp8_sdwa v[194:195], v195 src0_sel:WORD_1
	v_pk_add_f32 v[126:127], v[126:127], v[150:151]
	v_pk_add_f32 v[152:153], v[154:155], v[152:153]
	v_pk_add_f32 v[154:155], v[166:167], v[230:231]
	v_pk_fma_f32 v[98:99], v[128:129], s[2:3], v[98:99] op_sel_hi:[1,0,1]
	v_add_f32_e32 v67, v97, v67
	v_cvt_pk_f32_fp8_sdwa v[206:207], v207 src0_sel:WORD_1
	v_pk_add_f32 v[126:127], v[126:127], v[156:157]
	v_pk_add_f32 v[148:149], v[152:153], v[240:241]
	v_pk_add_f32 v[152:153], v[154:155], v[242:243]
	v_add_f32_e32 v67, v98, v67
	v_cvt_pk_f32_fp8_sdwa v[212:213], v213 src0_sel:WORD_1
	v_pk_add_f32 v[126:127], v[126:127], v[184:185]
	v_pk_fma_f32 v[108:109], v[152:153], s[2:3], v[108:109] op_sel_hi:[1,0,1]
	v_add_f32_e32 v67, v99, v67
	v_cvt_pk_f32_fp8_e32 v[220:221], v196
	v_cvt_pk_f32_fp8_sdwa v[218:219], v219 src0_sel:WORD_1
	v_pk_add_f32 v[126:127], v[126:127], v[192:193]
	v_add_f32_e32 v67, v108, v67
	v_pk_add_f32 v[132:133], v[132:133], v[194:195]
	v_cvt_pk_f32_fp8_e32 v[194:195], v198
	v_pk_fma_f32 v[110:111], v[126:127], s[2:3], v[110:111] op_sel_hi:[1,0,1]
	v_add_f32_e32 v67, v109, v67
	v_cvt_pk_f32_fp8_sdwa v[176:177], v196 src0_sel:WORD_1
	s_waitcnt vmcnt(0)
	v_cvt_pk_f32_fp8_e32 v[150:151], v200
	v_pk_add_f32 v[130:131], v[130:131], v[206:207]
	v_add_f32_e32 v67, v110, v67
	v_cvt_pk_f32_fp8_sdwa v[236:237], v198 src0_sel:WORD_1
	v_pk_add_f32 v[138:139], v[180:181], v[138:139]
	v_pk_add_f32 v[130:131], v[130:131], v[212:213]
	v_pk_fma_f32 v[104:105], v[148:149], s[2:3], v[104:105] op_sel_hi:[1,0,1]
	v_add_f32_e32 v67, v111, v67
	v_cvt_pk_f32_fp8_sdwa v[180:181], v200 src0_sel:WORD_1
	v_pk_add_f32 v[138:139], v[138:139], v[220:221]
	v_pk_add_f32 v[130:131], v[130:131], v[218:219]
	v_add_f32_e32 v67, v104, v67
	v_cvt_pk_f32_fp8_e32 v[188:189], v199
	v_pk_add_f32 v[182:183], v[182:183], v[244:245]
	v_pk_add_f32 v[138:139], v[138:139], v[194:195]
	v_pk_fma_f32 v[106:107], v[130:131], s[2:3], v[106:107] op_sel_hi:[1,0,1]
	v_add_f32_e32 v67, v105, v67
	v_cvt_pk_f32_fp8_sdwa v[196:197], v197 src0_sel:WORD_1
	v_cvt_pk_f32_fp8_e32 v[244:245], v201
	v_pk_add_f32 v[156:157], v[182:183], v[176:177]
	v_pk_add_f32 v[138:139], v[138:139], v[150:151]
	v_add_f32_e32 v67, v106, v67
	v_cvt_pk_f32_fp8_sdwa v[198:199], v199 src0_sel:WORD_1
	v_pk_add_f32 v[156:157], v[156:157], v[236:237]
	v_pk_fma_f32 v[112:113], v[138:139], s[2:3], v[112:113] op_sel_hi:[1,0,1]
	v_add_f32_e32 v67, v107, v67
	v_cvt_pk_f32_fp8_sdwa v[200:201], v201 src0_sel:WORD_1
	v_pk_add_f32 v[150:151], v[156:157], v[180:181]
	v_add_f32_e32 v67, v112, v67
	v_pk_add_f32 v[134:135], v[134:135], v[188:189]
	v_pk_fma_f32 v[114:115], v[150:151], s[2:3], v[114:115] op_sel_hi:[1,0,1]
	v_add_f32_e32 v67, v113, v67
	v_pk_add_f32 v[132:133], v[132:133], v[196:197]
	v_pk_add_f32 v[134:135], v[134:135], v[244:245]
	v_add_f32_e32 v67, v114, v67
	v_pk_add_f32 v[132:133], v[132:133], v[198:199]
	v_pk_fma_f32 v[84:85], v[134:135], s[2:3], v[84:85] op_sel_hi:[1,0,1]
	v_add_f32_e32 v67, v115, v67
	v_pk_add_f32 v[132:133], v[132:133], v[200:201]
	v_add_f32_e32 v67, v84, v67
	v_pk_fma_f32 v[86:87], v[132:133], s[2:3], v[86:87] op_sel_hi:[1,0,1]
	v_add_f32_e32 v67, v85, v67
	v_add_f32_e32 v67, v86, v67
	v_add_f32_e32 v67, v87, v67
	v_mov_b32_e32 v73, v67
	s_nop 1
	v_permlane32_swap_b32_e32 v73, v67
	s_waitcnt lgkmcnt(0)
	v_add_f32_e32 v67, v67, v73
	v_mov_b32_e32 v73, v67
	s_nop 1
	v_permlane16_swap_b32_e32 v73, v67
	s_waitcnt lgkmcnt(0)
	v_add_f32_e32 v67, v67, v73
	s_nop 1
	v_mov_b32_dpp v73, v67 row_ror:8 row_mask:0xf bank_mask:0xf
	s_waitcnt lgkmcnt(0)
	v_add_f32_e32 v67, v67, v73
	s_nop 1
	v_mov_b32_dpp v73, v67 row_shr:4 row_mask:0xf bank_mask:0xa
	v_mov_b32_dpp v73, v67 row_shl:4 row_mask:0xf bank_mask:0x5
	s_waitcnt lgkmcnt(0)
	v_add_f32_e32 v67, v67, v73
	s_nop 1
	v_mov_b32_dpp v73, v67 quad_perm:[2,3,0,1] row_mask:0xf bank_mask:0xf
	s_waitcnt lgkmcnt(0)
	v_add_f32_e32 v67, v67, v73
	s_nop 1
	v_mov_b32_dpp v73, v67 quad_perm:[1,0,3,2] row_mask:0xf bank_mask:0xf
	s_waitcnt lgkmcnt(0)
	v_add_f32_e32 v67, v67, v73
	v_mul_f32_e32 v124, 0x3a000000, v67
	v_pk_add_f32 v[92:93], v[92:93], v[124:125] op_sel_hi:[1,0] neg_lo:[0,1] neg_hi:[0,1]
	v_pk_add_f32 v[94:95], v[94:95], v[124:125] op_sel_hi:[1,0] neg_lo:[0,1] neg_hi:[0,1]
	v_pk_add_f32 v[88:89], v[88:89], v[124:125] op_sel_hi:[1,0] neg_lo:[0,1] neg_hi:[0,1]
	v_pk_add_f32 v[90:91], v[90:91], v[124:125] op_sel_hi:[1,0] neg_lo:[0,1] neg_hi:[0,1]
	v_pk_add_f32 v[100:101], v[100:101], v[124:125] op_sel_hi:[1,0] neg_lo:[0,1] neg_hi:[0,1]
	v_pk_add_f32 v[102:103], v[102:103], v[124:125] op_sel_hi:[1,0] neg_lo:[0,1] neg_hi:[0,1]
	v_pk_add_f32 v[96:97], v[96:97], v[124:125] op_sel_hi:[1,0] neg_lo:[0,1] neg_hi:[0,1]
	v_pk_add_f32 v[98:99], v[98:99], v[124:125] op_sel_hi:[1,0] neg_lo:[0,1] neg_hi:[0,1]
	v_pk_add_f32 v[108:109], v[108:109], v[124:125] op_sel_hi:[1,0] neg_lo:[0,1] neg_hi:[0,1]
	v_pk_add_f32 v[110:111], v[110:111], v[124:125] op_sel_hi:[1,0] neg_lo:[0,1] neg_hi:[0,1]
	v_pk_add_f32 v[104:105], v[104:105], v[124:125] op_sel_hi:[1,0] neg_lo:[0,1] neg_hi:[0,1]
	v_pk_add_f32 v[106:107], v[106:107], v[124:125] op_sel_hi:[1,0] neg_lo:[0,1] neg_hi:[0,1]
	v_pk_add_f32 v[112:113], v[112:113], v[124:125] op_sel_hi:[1,0] neg_lo:[0,1] neg_hi:[0,1]
	v_pk_add_f32 v[114:115], v[114:115], v[124:125] op_sel_hi:[1,0] neg_lo:[0,1] neg_hi:[0,1]
	v_pk_add_f32 v[84:85], v[84:85], v[124:125] op_sel_hi:[1,0] neg_lo:[0,1] neg_hi:[0,1]
	v_pk_add_f32 v[86:87], v[86:87], v[124:125] op_sel_hi:[1,0] neg_lo:[0,1] neg_hi:[0,1]
	v_pk_mul_f32 v[124:125], v[92:93], v[92:93]
	v_pk_mul_f32 v[126:127], v[94:95], v[94:95]
	v_add_f32_e32 v67, v124, v125
	v_add_f32_e32 v67, v126, v67
	v_pk_mul_f32 v[128:129], v[88:89], v[88:89]
	v_add_f32_e32 v67, v127, v67
	v_add_f32_e32 v67, v128, v67
	v_pk_mul_f32 v[130:131], v[90:91], v[90:91]
	v_add_f32_e32 v67, v129, v67
	v_add_f32_e32 v67, v130, v67
	v_pk_mul_f32 v[132:133], v[100:101], v[100:101]
	v_add_f32_e32 v67, v131, v67
	v_add_f32_e32 v67, v132, v67
	v_pk_mul_f32 v[134:135], v[102:103], v[102:103]
	v_add_f32_e32 v67, v133, v67
	v_add_f32_e32 v67, v134, v67
	v_pk_mul_f32 v[136:137], v[96:97], v[96:97]
	v_add_f32_e32 v67, v135, v67
	v_add_f32_e32 v67, v136, v67
	v_pk_mul_f32 v[138:139], v[98:99], v[98:99]
	v_add_f32_e32 v67, v137, v67
	v_add_f32_e32 v67, v138, v67
	v_pk_mul_f32 v[140:141], v[108:109], v[108:109]
	v_add_f32_e32 v67, v139, v67
	v_add_f32_e32 v67, v140, v67
	v_pk_mul_f32 v[142:143], v[110:111], v[110:111]
	v_add_f32_e32 v67, v141, v67
	v_add_f32_e32 v67, v142, v67
	v_pk_mul_f32 v[144:145], v[104:105], v[104:105]
	v_add_f32_e32 v67, v143, v67
	v_add_f32_e32 v67, v144, v67
	v_pk_mul_f32 v[146:147], v[106:107], v[106:107]
	v_add_f32_e32 v67, v145, v67
	v_add_f32_e32 v67, v146, v67
	v_pk_mul_f32 v[148:149], v[112:113], v[112:113]
	v_add_f32_e32 v67, v147, v67
	v_add_f32_e32 v67, v148, v67
	v_pk_mul_f32 v[150:151], v[114:115], v[114:115]
	v_add_f32_e32 v67, v149, v67
	v_add_f32_e32 v67, v150, v67
	v_pk_mul_f32 v[152:153], v[84:85], v[84:85]
	v_add_f32_e32 v67, v151, v67
	v_add_f32_e32 v67, v152, v67
	v_pk_mul_f32 v[154:155], v[86:87], v[86:87]
	v_add_f32_e32 v67, v153, v67
	v_add_f32_e32 v67, v154, v67
	v_add_f32_e32 v67, v155, v67
	v_mov_b32_e32 v73, v67
	s_nop 1
	v_permlane32_swap_b32_e32 v73, v67
	s_waitcnt lgkmcnt(0)
	v_add_f32_e32 v67, v67, v73
	v_mov_b32_e32 v73, v67
	s_nop 1
	v_permlane16_swap_b32_e32 v73, v67
	s_waitcnt lgkmcnt(0)
	v_add_f32_e32 v67, v67, v73
	s_nop 1
	v_mov_b32_dpp v73, v67 row_ror:8 row_mask:0xf bank_mask:0xf
	s_waitcnt lgkmcnt(0)
	v_add_f32_e32 v67, v67, v73
	s_nop 1
	v_mov_b32_dpp v73, v67 row_shr:4 row_mask:0xf bank_mask:0xa
	v_mov_b32_dpp v73, v67 row_shl:4 row_mask:0xf bank_mask:0x5
	s_waitcnt lgkmcnt(0)
	v_add_f32_e32 v67, v67, v73
	s_nop 1
	v_mov_b32_dpp v73, v67 quad_perm:[2,3,0,1] row_mask:0xf bank_mask:0xf
	s_waitcnt lgkmcnt(0)
	v_add_f32_e32 v67, v67, v73
	s_nop 1
	v_mov_b32_dpp v73, v67 quad_perm:[1,0,3,2] row_mask:0xf bank_mask:0xf
	s_waitcnt lgkmcnt(0)
	v_add_f32_e32 v67, v67, v73
	v_fmamk_f32 v67, v67, 0x3a000000, v123
	v_mul_f32_e32 v73, 0x4b800000, v67
	v_cmp_gt_f32_e32 vcc, s6, v67
	s_nop 1
	v_cndmask_b32_e32 v67, v67, v73, vcc
	v_rsq_f32_e32 v67, v67
	s_nop 0
	v_mul_f32_e32 v73, 0x45800000, v67
	v_cndmask_b32_e32 v124, v67, v73, vcc
	v_pk_mul_f32 v[92:93], v[92:93], v[124:125] op_sel_hi:[1,0]
	v_pk_mul_f32 v[94:95], v[94:95], v[124:125] op_sel_hi:[1,0]
	v_pk_mul_f32 v[88:89], v[88:89], v[124:125] op_sel_hi:[1,0]
	v_pk_mul_f32 v[90:91], v[90:91], v[124:125] op_sel_hi:[1,0]
	v_pk_mul_f32 v[100:101], v[100:101], v[124:125] op_sel_hi:[1,0]
	v_pk_mul_f32 v[102:103], v[102:103], v[124:125] op_sel_hi:[1,0]
	v_pk_mul_f32 v[96:97], v[96:97], v[124:125] op_sel_hi:[1,0]
	v_pk_mul_f32 v[98:99], v[98:99], v[124:125] op_sel_hi:[1,0]
	v_pk_mul_f32 v[108:109], v[108:109], v[124:125] op_sel_hi:[1,0]
	v_pk_mul_f32 v[110:111], v[110:111], v[124:125] op_sel_hi:[1,0]
	v_pk_mul_f32 v[104:105], v[104:105], v[124:125] op_sel_hi:[1,0]
	v_pk_mul_f32 v[106:107], v[106:107], v[124:125] op_sel_hi:[1,0]
	v_pk_mul_f32 v[112:113], v[112:113], v[124:125] op_sel_hi:[1,0]
	v_pk_mul_f32 v[114:115], v[114:115], v[124:125] op_sel_hi:[1,0]
	v_pk_mul_f32 v[126:127], v[84:85], v[124:125] op_sel_hi:[1,0]
	v_pk_mul_f32 v[124:125], v[86:87], v[124:125] op_sel_hi:[1,0]
	v_pk_fma_f32 v[86:87], v[62:63], v[94:95], v[58:59]
	v_pk_fma_f32 v[84:85], v[60:61], v[92:93], v[56:57]
	v_pk_fma_f32 v[90:91], v[54:55], v[90:91], v[50:51]
	v_pk_fma_f32 v[88:89], v[52:53], v[88:89], v[48:49]
	v_pk_fma_f32 v[94:95], v[46:47], v[102:103], v[42:43]
	v_pk_fma_f32 v[92:93], v[44:45], v[100:101], v[40:41]
	v_pk_fma_f32 v[98:99], v[38:39], v[98:99], v[34:35]
	v_pk_fma_f32 v[96:97], v[36:37], v[96:97], v[32:33]
	v_pk_fma_f32 v[102:103], v[30:31], v[110:111], v[26:27]
	v_pk_fma_f32 v[100:101], v[28:29], v[108:109], v[24:25]
	v_pk_fma_f32 v[106:107], v[22:23], v[106:107], v[18:19]
	v_pk_fma_f32 v[104:105], v[20:21], v[104:105], v[16:17]
	v_pk_fma_f32 v[110:111], v[14:15], v[114:115], v[10:11]
	v_pk_fma_f32 v[108:109], v[12:13], v[112:113], v[8:9]
	v_pk_fma_f32 v[114:115], v[6:7], v[124:125], v[2:3]
	v_pk_fma_f32 v[112:113], v[4:5], v[126:127], v[0:1]
	global_store_dwordx4 v[82:83], v[84:87], off
	global_store_dwordx4 v[82:83], v[88:91], off offset:16
	global_store_dwordx4 v[82:83], v[92:95], off offset:2048
	global_store_dwordx4 v[82:83], v[96:99], off offset:2064
	global_store_dwordx4 v[80:81], v[100:103], off
	global_store_dwordx4 v[80:81], v[104:107], off offset:16
	global_store_dwordx4 v[78:79], v[108:111], off
	global_store_dwordx4 v[78:79], v[112:115], off offset:16
	s_andn2_b64 exec, exec, s[0:1]
	s_cbranch_execnz .LBB0_1734
